# v15 + code placement: the attention step loop and the GEMM K-loop heads aligned to 64 bytes (s_nop fill)
# speedup vs baseline: 1.0036x; 1.0036x over previous
.LBB0_260:
	ds_read_b128 v[2:5], v143
	ds_read_b128 v[6:9], v143 offset:1024
	ds_read_b128 v[10:13], v143 offset:2048
	ds_read_b128 v[14:17], v143 offset:3072
	ds_read_b128 v[18:21], v144
	ds_read_b128 v[22:25], v144 offset:1024
	ds_read_b128 v[26:29], v144 offset:2048
	ds_read_b128 v[30:33], v144 offset:3072
	s_add_i32 s44, s10, 0x180
	s_add_i32 s45, s10, 0x80
	s_add_i32 s30, s10, 0x100
	s_add_i32 s31, s46, 0x100
	s_mov_b32 s12, s38
	s_mov_b32 m0, s74
	ds_read_b128 v[34:37], v145
	ds_read_b128 v[38:41], v145 offset:1024
	ds_read_b128 v[42:45], v145 offset:2048
	ds_read_b128 v[46:49], v145 offset:3072
	ds_read_b128 v[50:53], v145 offset:4096
	ds_read_b128 v[54:57], v145 offset:5120
	ds_read_b128 v[58:61], v145 offset:6144
	ds_read_b128 v[62:65], v145 offset:7168
	buffer_load_dwordx4 v140, s[12:15], s45 offen lds
	s_mov_b32 m0, s75
	s_nop 0
	buffer_load_dwordx4 v142, s[12:15], s45 offen lds
	s_waitcnt vmcnt(18)
	s_waitcnt lgkmcnt(0)
	s_barrier
	s_setprio 1
	s_waitcnt lgkmcnt(0)
	v_mfma_f32_16x16x32_bf16 v[86:89], v[10:13], v[50:53], 0
	v_mfma_f32_16x16x32_bf16 v[90:93], v[14:17], v[54:57], v[86:89]
	v_mfma_f32_16x16x32_bf16 v[86:89], v[2:5], v[58:61], 0
	v_mfma_f32_16x16x32_bf16 v[66:69], v[2:5], v[34:37], 0
	v_mfma_f32_16x16x32_bf16 v[70:73], v[10:13], v[34:37], 0
	v_mfma_f32_16x16x32_bf16 v[74:77], v[2:5], v[42:45], 0
	v_mfma_f32_16x16x32_bf16 v[78:81], v[10:13], v[42:45], 0
	v_mfma_f32_16x16x32_bf16 v[82:85], v[2:5], v[50:53], 0
	v_mfma_f32_16x16x32_bf16 v[94:97], v[6:9], v[62:65], v[86:89]
	v_mfma_f32_16x16x32_bf16 v[86:89], v[10:13], v[58:61], 0
	v_mfma_f32_16x16x32_bf16 v[66:69], v[6:9], v[38:41], v[66:69]
	v_mfma_f32_16x16x32_bf16 v[70:73], v[14:17], v[38:41], v[70:73]
	v_mfma_f32_16x16x32_bf16 v[74:77], v[6:9], v[46:49], v[74:77]
	v_mfma_f32_16x16x32_bf16 v[78:81], v[14:17], v[46:49], v[78:81]
	v_mfma_f32_16x16x32_bf16 v[82:85], v[6:9], v[54:57], v[82:85]
	v_mfma_f32_16x16x32_bf16 v[106:109], v[14:17], v[62:65], v[86:89]
	s_setprio 0
	s_setprio 1
	v_mfma_f32_16x16x32_bf16 v[86:89], v[18:21], v[34:37], 0
	v_mfma_f32_16x16x32_bf16 v[34:37], v[26:29], v[34:37], 0
	v_mfma_f32_16x16x32_bf16 v[110:113], v[22:25], v[38:41], v[86:89]
	v_mfma_f32_16x16x32_bf16 v[34:37], v[30:33], v[38:41], v[34:37]
	v_mfma_f32_16x16x32_bf16 v[38:41], v[18:21], v[42:45], 0
	v_mfma_f32_16x16x32_bf16 v[42:45], v[26:29], v[42:45], 0
	v_mfma_f32_16x16x32_bf16 v[38:41], v[22:25], v[46:49], v[38:41]
	v_mfma_f32_16x16x32_bf16 v[42:45], v[30:33], v[46:49], v[42:45]
	v_mfma_f32_16x16x32_bf16 v[46:49], v[18:21], v[50:53], 0
	v_mfma_f32_16x16x32_bf16 v[50:53], v[26:29], v[50:53], 0
	v_mfma_f32_16x16x32_bf16 v[46:49], v[22:25], v[54:57], v[46:49]
	v_mfma_f32_16x16x32_bf16 v[50:53], v[30:33], v[54:57], v[50:53]
	v_mfma_f32_16x16x32_bf16 v[54:57], v[18:21], v[58:61], 0
	v_mfma_f32_16x16x32_bf16 v[148:151], v[22:25], v[62:65], v[54:57]
	v_mfma_f32_16x16x32_bf16 v[54:57], v[26:29], v[58:61], 0
	v_mfma_f32_16x16x32_bf16 v[58:61], v[30:33], v[62:65], v[54:57]
	s_setprio 0
	s_barrier
	s_mov_b32 m0, s54
	s_nop 3
	ds_read_b128 v[54:57], v145 offset:16384
	ds_read_b128 v[62:65], v145 offset:17408
	ds_read_b128 v[86:89], v145 offset:18432
	ds_read_b128 v[98:101], v145 offset:19456
	ds_read_b128 v[102:105], v145 offset:20480
	ds_read_b128 v[114:117], v145 offset:21504
	ds_read_b128 v[118:121], v145 offset:22528
	ds_read_b128 v[122:125], v145 offset:23552
	buffer_load_dwordx4 v1, s[12:15], s31 offen lds
	s_mov_b32 m0, s55
	s_nop 0
	buffer_load_dwordx4 v138, s[12:15], s31 offen lds
	s_add_i32 s31, s46, 0x40100
	s_mov_b32 m0, s56
	s_nop 0
	buffer_load_dwordx4 v1, s[12:15], s31 offen lds
	s_mov_b32 m0, s57
	s_nop 0
	buffer_load_dwordx4 v138, s[12:15], s31 offen lds
	s_mov_b32 m0, s53
	s_nop 0
	buffer_load_dwordx4 v139, s[12:15], s30 offen lds
	s_mov_b32 m0, s58
	s_nop 0
	buffer_load_dwordx4 v141, s[12:15], s30 offen lds
	s_waitcnt vmcnt(22)
	s_waitcnt lgkmcnt(0)
	s_barrier
	s_setprio 1
	s_waitcnt lgkmcnt(0)
	v_mfma_f32_16x16x32_bf16 v[126:129], v[2:5], v[54:57], 0
	v_mfma_f32_16x16x32_bf16 v[152:155], v[6:9], v[62:65], v[126:129]
	v_mfma_f32_16x16x32_bf16 v[126:129], v[10:13], v[54:57], 0
	v_mfma_f32_16x16x32_bf16 v[156:159], v[14:17], v[62:65], v[126:129]
	v_mfma_f32_16x16x32_bf16 v[126:129], v[2:5], v[86:89], 0
	v_mfma_f32_16x16x32_bf16 v[160:163], v[6:9], v[98:101], v[126:129]
	v_mfma_f32_16x16x32_bf16 v[126:129], v[10:13], v[86:89], 0
	v_mfma_f32_16x16x32_bf16 v[164:167], v[14:17], v[98:101], v[126:129]
	v_mfma_f32_16x16x32_bf16 v[126:129], v[2:5], v[102:105], 0
	v_mfma_f32_16x16x32_bf16 v[2:5], v[2:5], v[118:121], 0
	v_mfma_f32_16x16x32_bf16 v[168:171], v[6:9], v[114:117], v[126:129]
	v_mfma_f32_16x16x32_bf16 v[2:5], v[6:9], v[122:125], v[2:5]
	v_mfma_f32_16x16x32_bf16 v[6:9], v[10:13], v[118:121], 0
	v_mfma_f32_16x16x32_bf16 v[126:129], v[10:13], v[102:105], 0
	v_mfma_f32_16x16x32_bf16 v[10:13], v[14:17], v[122:125], v[6:9]
	v_mfma_f32_16x16x32_bf16 v[172:175], v[14:17], v[114:117], v[126:129]
	s_setprio 0
	s_setprio 1
	v_mfma_f32_16x16x32_bf16 v[6:9], v[18:21], v[54:57], 0
	v_mfma_f32_16x16x32_bf16 v[14:17], v[22:25], v[62:65], v[6:9]
	v_mfma_f32_16x16x32_bf16 v[6:9], v[26:29], v[54:57], 0
	v_mfma_f32_16x16x32_bf16 v[62:65], v[30:33], v[62:65], v[6:9]
	v_mfma_f32_16x16x32_bf16 v[6:9], v[18:21], v[86:89], 0
	v_mfma_f32_16x16x32_bf16 v[176:179], v[22:25], v[98:101], v[6:9]
	v_mfma_f32_16x16x32_bf16 v[6:9], v[26:29], v[86:89], 0
	v_mfma_f32_16x16x32_bf16 v[180:183], v[30:33], v[98:101], v[6:9]
	v_mfma_f32_16x16x32_bf16 v[6:9], v[18:21], v[102:105], 0
	v_mfma_f32_16x16x32_bf16 v[184:187], v[22:25], v[114:117], v[6:9]
	v_mfma_f32_16x16x32_bf16 v[6:9], v[26:29], v[102:105], 0
	v_mfma_f32_16x16x32_bf16 v[188:191], v[30:33], v[114:117], v[6:9]
	v_mfma_f32_16x16x32_bf16 v[6:9], v[18:21], v[118:121], 0
	v_mfma_f32_16x16x32_bf16 v[192:195], v[22:25], v[122:125], v[6:9]
	v_mfma_f32_16x16x32_bf16 v[6:9], v[26:29], v[118:121], 0
	v_mfma_f32_16x16x32_bf16 v[196:199], v[30:33], v[122:125], v[6:9]
	s_setprio 0
	s_barrier
; template <class Epi, class Sched>
; __device__ __forceinline__ void gemm_phase(PG8_LAS unsigned char* lds, const void* wsbase, const int K, const int ldb, const Sched& S, const Epi& E) {
;     ...
;         PG8_ITER(0, PG8_FIRSTW + 2 + Epi::NVM, PG8_FIRSTW + 6 + Epi::NVM, PG8_FIRSTW + 2 + Epi::NVM, PG8_FIRSTW + 6);
;         for (int t = 2; t < nt; t += 2) PG8_ITER(t, 8 + PG8_SLK1, 8 + PG8_SLK2, 8 + PG8_SLK1, 8 + PG8_SLK2);
	s_nop 4
	ds_read_b128 v[6:9], v146
	ds_read_b128 v[26:29], v146 offset:1024
	ds_read_b128 v[30:33], v146 offset:2048
	ds_read_b128 v[200:203], v146 offset:3072
	ds_read_b128 v[204:207], v147
	ds_read_b128 v[208:211], v147 offset:1024
	ds_read_b128 v[212:215], v147 offset:2048
	ds_read_b128 v[216:219], v147 offset:3072
	s_mov_b32 m0, s59
	ds_read_b128 v[18:21], v145 offset:32768
	ds_read_b128 v[22:25], v145 offset:33792
	ds_read_b128 v[220:223], v145 offset:34816
	ds_read_b128 v[224:227], v145 offset:35840
	ds_read_b128 v[232:235], v145 offset:36864
	ds_read_b128 v[236:239], v145 offset:37888
	ds_read_b128 v[240:243], v145 offset:38912
	ds_read_b128 v[244:247], v145 offset:39936
	buffer_load_dwordx4 v140, s[12:15], s30 offen lds
	s_mov_b32 m0, s60
	s_nop 0
	buffer_load_dwordx4 v142, s[12:15], s30 offen lds
	s_waitcnt vmcnt(18)
	s_waitcnt lgkmcnt(0)
	s_barrier
	s_setprio 1
	s_waitcnt lgkmcnt(0)
	v_mfma_f32_16x16x32_bf16 v[54:57], v[6:9], v[18:21], v[66:69]
	v_mfma_f32_16x16x32_bf16 v[118:121], v[26:29], v[22:25], v[54:57]
	v_mfma_f32_16x16x32_bf16 v[54:57], v[30:33], v[18:21], v[70:73]
	v_mfma_f32_16x16x32_bf16 v[114:117], v[200:203], v[22:25], v[54:57]
	v_mfma_f32_16x16x32_bf16 v[54:57], v[6:9], v[220:223], v[74:77]
	v_mfma_f32_16x16x32_bf16 v[102:105], v[26:29], v[224:227], v[54:57]
	v_mfma_f32_16x16x32_bf16 v[54:57], v[30:33], v[220:223], v[78:81]
	v_mfma_f32_16x16x32_bf16 v[98:101], v[200:203], v[224:227], v[54:57]
	v_mfma_f32_16x16x32_bf16 v[54:57], v[6:9], v[232:235], v[82:85]
	v_mfma_f32_16x16x32_bf16 v[86:89], v[26:29], v[236:239], v[54:57]
	v_mfma_f32_16x16x32_bf16 v[54:57], v[30:33], v[232:235], v[90:93]
	v_mfma_f32_16x16x32_bf16 v[82:85], v[200:203], v[236:239], v[54:57]
	v_mfma_f32_16x16x32_bf16 v[54:57], v[6:9], v[240:243], v[94:97]
	v_mfma_f32_16x16x32_bf16 v[66:69], v[26:29], v[244:247], v[54:57]
	v_mfma_f32_16x16x32_bf16 v[54:57], v[30:33], v[240:243], v[106:109]
	v_mfma_f32_16x16x32_bf16 v[54:57], v[200:203], v[244:247], v[54:57]
	s_setprio 0
	s_setprio 1
	v_mfma_f32_16x16x32_bf16 v[70:73], v[204:207], v[18:21], v[110:113]
	v_mfma_f32_16x16x32_bf16 v[18:21], v[212:215], v[18:21], v[34:37]
	v_mfma_f32_16x16x32_bf16 v[122:125], v[216:219], v[22:25], v[18:21]
	v_mfma_f32_16x16x32_bf16 v[18:21], v[204:207], v[220:223], v[38:41]
	v_mfma_f32_16x16x32_bf16 v[110:113], v[208:211], v[224:227], v[18:21]
	v_mfma_f32_16x16x32_bf16 v[18:21], v[212:215], v[220:223], v[42:45]
	v_mfma_f32_16x16x32_bf16 v[106:109], v[216:219], v[224:227], v[18:21]
	v_mfma_f32_16x16x32_bf16 v[18:21], v[204:207], v[232:235], v[46:49]
	v_mfma_f32_16x16x32_bf16 v[94:97], v[208:211], v[236:239], v[18:21]
	v_mfma_f32_16x16x32_bf16 v[18:21], v[212:215], v[232:235], v[50:53]
	v_mfma_f32_16x16x32_bf16 v[90:93], v[216:219], v[236:239], v[18:21]
	v_mfma_f32_16x16x32_bf16 v[18:21], v[204:207], v[240:243], v[148:151]
	v_mfma_f32_16x16x32_bf16 v[78:81], v[208:211], v[244:247], v[18:21]
	v_mfma_f32_16x16x32_bf16 v[18:21], v[212:215], v[240:243], v[58:61]
	v_mfma_f32_16x16x32_bf16 v[126:129], v[208:211], v[22:25], v[70:73]
	v_mfma_f32_16x16x32_bf16 v[70:73], v[216:219], v[244:247], v[18:21]
	s_setprio 0
	s_barrier
	s_mov_b32 m0, s66
	s_add_i32 s30, s46, 0x180
	ds_read_b128 v[42:45], v145 offset:49152
	ds_read_b128 v[46:49], v145 offset:50176
	ds_read_b128 v[148:151], v145 offset:51200
	ds_read_b128 v[220:223], v145 offset:52224
	ds_read_b128 v[224:227], v145 offset:53248
	ds_read_b128 v[232:235], v145 offset:54272
	ds_read_b128 v[236:239], v145 offset:55296
	ds_read_b128 v[240:243], v145 offset:56320
	buffer_load_dwordx4 v1, s[12:15], s30 offen lds
	s_mov_b32 m0, s68
	s_nop 0
	buffer_load_dwordx4 v138, s[12:15], s30 offen lds
	s_add_i32 s30, s46, 0x40180
	s_mov_b32 m0, s72
	s_nop 0
	buffer_load_dwordx4 v1, s[12:15], s30 offen lds
	s_mov_b32 m0, s73
	s_nop 0
	buffer_load_dwordx4 v138, s[12:15], s30 offen lds
	s_mov_b32 m0, s69
	s_nop 0
	buffer_load_dwordx4 v139, s[12:15], s44 offen lds
	s_mov_b32 m0, s70
	s_nop 0
	buffer_load_dwordx4 v141, s[12:15], s44 offen lds
	s_waitcnt vmcnt(14)
	s_waitcnt lgkmcnt(0)
	s_barrier
	s_setprio 1
	s_waitcnt lgkmcnt(0)
	v_mfma_f32_16x16x32_bf16 v[18:21], v[6:9], v[42:45], v[152:155]
	v_mfma_f32_16x16x32_bf16 v[58:61], v[26:29], v[46:49], v[18:21]
	v_mfma_f32_16x16x32_bf16 v[18:21], v[30:33], v[42:45], v[156:159]
	v_mfma_f32_16x16x32_bf16 v[50:53], v[200:203], v[46:49], v[18:21]
	v_mfma_f32_16x16x32_bf16 v[18:21], v[6:9], v[148:151], v[160:163]
	v_mfma_f32_16x16x32_bf16 v[38:41], v[26:29], v[220:223], v[18:21]
	v_mfma_f32_16x16x32_bf16 v[18:21], v[30:33], v[148:151], v[164:167]
	v_mfma_f32_16x16x32_bf16 v[34:37], v[200:203], v[220:223], v[18:21]
	v_mfma_f32_16x16x32_bf16 v[18:21], v[6:9], v[224:227], v[168:171]
	v_mfma_f32_16x16x32_bf16 v[2:5], v[6:9], v[236:239], v[2:5]
	v_mfma_f32_16x16x32_bf16 v[22:25], v[26:29], v[232:235], v[18:21]
	v_mfma_f32_16x16x32_bf16 v[18:21], v[30:33], v[224:227], v[172:175]
	v_mfma_f32_16x16x32_bf16 v[6:9], v[26:29], v[240:243], v[2:5]
	v_mfma_f32_16x16x32_bf16 v[2:5], v[30:33], v[236:239], v[10:13]
	v_mfma_f32_16x16x32_bf16 v[18:21], v[200:203], v[232:235], v[18:21]
	v_mfma_f32_16x16x32_bf16 v[2:5], v[200:203], v[240:243], v[2:5]
	s_setprio 0
	s_setprio 1
	v_mfma_f32_16x16x32_bf16 v[10:13], v[204:207], v[42:45], v[14:17]
	v_mfma_f32_16x16x32_bf16 v[74:77], v[208:211], v[46:49], v[10:13]
	v_mfma_f32_16x16x32_bf16 v[10:13], v[212:215], v[42:45], v[62:65]
	v_mfma_f32_16x16x32_bf16 v[62:65], v[216:219], v[46:49], v[10:13]
	v_mfma_f32_16x16x32_bf16 v[10:13], v[204:207], v[148:151], v[176:179]
	v_mfma_f32_16x16x32_bf16 v[46:49], v[208:211], v[220:223], v[10:13]
	v_mfma_f32_16x16x32_bf16 v[10:13], v[212:215], v[148:151], v[180:183]
	v_mfma_f32_16x16x32_bf16 v[42:45], v[216:219], v[220:223], v[10:13]
	v_mfma_f32_16x16x32_bf16 v[10:13], v[204:207], v[224:227], v[184:187]
	v_mfma_f32_16x16x32_bf16 v[30:33], v[208:211], v[232:235], v[10:13]
	v_mfma_f32_16x16x32_bf16 v[10:13], v[212:215], v[224:227], v[188:191]
	v_mfma_f32_16x16x32_bf16 v[26:29], v[216:219], v[232:235], v[10:13]
	v_mfma_f32_16x16x32_bf16 v[10:13], v[204:207], v[236:239], v[192:195]
	v_mfma_f32_16x16x32_bf16 v[14:17], v[208:211], v[240:243], v[10:13]
	v_mfma_f32_16x16x32_bf16 v[10:13], v[212:215], v[236:239], v[196:199]
	v_mfma_f32_16x16x32_bf16 v[10:13], v[216:219], v[240:243], v[10:13]
	s_setprio 0
	s_barrier
	s_add_i32 s44, s46, 0x200
	s_addk_i32 s10, 0x200
	s_mov_b32 s45, 0
	.p2alignl 6, 3212836864

.LBB0_369:
	ds_read_b128 v[2:5], v141
	ds_read_b128 v[6:9], v141 offset:1024
	ds_read_b128 v[10:13], v141 offset:2048
	ds_read_b128 v[14:17], v141 offset:3072
	ds_read_b128 v[18:21], v142
	ds_read_b128 v[22:25], v142 offset:1024
	ds_read_b128 v[26:29], v142 offset:2048
	ds_read_b128 v[30:33], v142 offset:3072
	s_add_i32 s3, s1, 0x100
	s_add_i32 s2, s1, 0x180
	s_add_i32 s30, s12, 0x100
	s_add_i32 s31, s1, 0x80
	s_mov_b32 m0, s65
	ds_read_b128 v[34:37], v143
	ds_read_b128 v[38:41], v143 offset:1024
	ds_read_b128 v[42:45], v143 offset:2048
	ds_read_b128 v[46:49], v143 offset:3072
	ds_read_b128 v[50:53], v143 offset:4096
	ds_read_b128 v[54:57], v143 offset:5120
	ds_read_b128 v[58:61], v143 offset:6144
	ds_read_b128 v[62:65], v143 offset:7168
	buffer_load_dwordx4 v138, s[16:19], s31 offen lds
	s_mov_b32 m0, s66
	s_nop 0
	buffer_load_dwordx4 v140, s[16:19], s31 offen lds
	s_waitcnt vmcnt(26)
	s_waitcnt lgkmcnt(0)
	s_barrier
	s_setprio 1
	s_waitcnt lgkmcnt(1)
	v_mfma_f32_16x16x32_bf16 v[90:93], v[2:5], v[58:61], 0
	v_mfma_f32_16x16x32_bf16 v[66:69], v[2:5], v[34:37], 0
	v_mfma_f32_16x16x32_bf16 v[70:73], v[10:13], v[34:37], 0
	v_mfma_f32_16x16x32_bf16 v[74:77], v[2:5], v[42:45], 0
	v_mfma_f32_16x16x32_bf16 v[78:81], v[10:13], v[42:45], 0
	v_mfma_f32_16x16x32_bf16 v[82:85], v[2:5], v[50:53], 0
	v_mfma_f32_16x16x32_bf16 v[86:89], v[10:13], v[50:53], 0
	s_waitcnt lgkmcnt(0)
	v_mfma_f32_16x16x32_bf16 v[98:101], v[6:9], v[62:65], v[90:93]
	v_mfma_f32_16x16x32_bf16 v[90:93], v[10:13], v[58:61], 0
	v_mfma_f32_16x16x32_bf16 v[66:69], v[6:9], v[38:41], v[66:69]
	v_mfma_f32_16x16x32_bf16 v[70:73], v[14:17], v[38:41], v[70:73]
	v_mfma_f32_16x16x32_bf16 v[74:77], v[6:9], v[46:49], v[74:77]
	v_mfma_f32_16x16x32_bf16 v[78:81], v[14:17], v[46:49], v[78:81]
	v_mfma_f32_16x16x32_bf16 v[82:85], v[6:9], v[54:57], v[82:85]
	v_mfma_f32_16x16x32_bf16 v[86:89], v[14:17], v[54:57], v[86:89]
	v_mfma_f32_16x16x32_bf16 v[102:105], v[14:17], v[62:65], v[90:93]
	s_setprio 0
	s_setprio 1
	v_mfma_f32_16x16x32_bf16 v[90:93], v[18:21], v[34:37], 0
	v_mfma_f32_16x16x32_bf16 v[34:37], v[26:29], v[34:37], 0
	v_mfma_f32_16x16x32_bf16 v[114:117], v[22:25], v[38:41], v[90:93]
	v_mfma_f32_16x16x32_bf16 v[34:37], v[30:33], v[38:41], v[34:37]
	v_mfma_f32_16x16x32_bf16 v[38:41], v[18:21], v[42:45], 0
	v_mfma_f32_16x16x32_bf16 v[42:45], v[26:29], v[42:45], 0
	v_mfma_f32_16x16x32_bf16 v[38:41], v[22:25], v[46:49], v[38:41]
	v_mfma_f32_16x16x32_bf16 v[42:45], v[30:33], v[46:49], v[42:45]
	v_mfma_f32_16x16x32_bf16 v[46:49], v[18:21], v[50:53], 0
	v_mfma_f32_16x16x32_bf16 v[50:53], v[26:29], v[50:53], 0
	v_mfma_f32_16x16x32_bf16 v[46:49], v[22:25], v[54:57], v[46:49]
	v_mfma_f32_16x16x32_bf16 v[50:53], v[30:33], v[54:57], v[50:53]
	v_mfma_f32_16x16x32_bf16 v[54:57], v[18:21], v[58:61], 0
	v_mfma_f32_16x16x32_bf16 v[58:61], v[26:29], v[58:61], 0
	v_mfma_f32_16x16x32_bf16 v[54:57], v[22:25], v[62:65], v[54:57]
	v_mfma_f32_16x16x32_bf16 v[58:61], v[30:33], v[62:65], v[58:61]
	s_setprio 0
	s_barrier
	s_mov_b32 m0, s51
	ds_read_b128 v[62:65], v143 offset:16384
	ds_read_b128 v[90:93], v143 offset:17408
	ds_read_b128 v[94:97], v143 offset:18432
	ds_read_b128 v[106:109], v143 offset:19456
	ds_read_b128 v[110:113], v143 offset:20480
	ds_read_b128 v[118:121], v143 offset:21504
	ds_read_b128 v[122:125], v143 offset:22528
	ds_read_b128 v[126:129], v143 offset:23552
	buffer_load_dwordx4 v1, s[16:19], s30 offen lds
	s_mov_b32 m0, s52
	s_nop 0
	buffer_load_dwordx4 v136, s[16:19], s30 offen lds
	s_add_i32 s30, s12, 0x100100
	s_mov_b32 m0, s53
	s_nop 0
	buffer_load_dwordx4 v1, s[16:19], s30 offen lds
	s_mov_b32 m0, s54
	s_nop 0
	buffer_load_dwordx4 v136, s[16:19], s30 offen lds
	s_mov_b32 m0, s50
	s_nop 0
	buffer_load_dwordx4 v137, s[16:19], s3 offen lds
	s_mov_b32 m0, s55
	s_nop 0
	buffer_load_dwordx4 v139, s[16:19], s3 offen lds
	s_waitcnt vmcnt(30)
	s_waitcnt lgkmcnt(0)
	s_barrier
	s_setprio 1
	s_waitcnt lgkmcnt(7)
	v_mfma_f32_16x16x32_bf16 v[154:157], v[2:5], v[62:65], 0
	s_waitcnt lgkmcnt(5)
	v_mfma_f32_16x16x32_bf16 v[162:165], v[2:5], v[94:97], 0
	s_waitcnt lgkmcnt(3)
	v_mfma_f32_16x16x32_bf16 v[170:173], v[2:5], v[110:113], 0
	s_waitcnt lgkmcnt(1)
	v_mfma_f32_16x16x32_bf16 v[2:5], v[2:5], v[122:125], 0
	v_mfma_f32_16x16x32_bf16 v[154:157], v[6:9], v[90:93], v[154:157]
	v_mfma_f32_16x16x32_bf16 v[162:165], v[6:9], v[106:109], v[162:165]
	v_mfma_f32_16x16x32_bf16 v[170:173], v[6:9], v[118:121], v[170:173]
	s_waitcnt lgkmcnt(0)
	v_mfma_f32_16x16x32_bf16 v[2:5], v[6:9], v[126:129], v[2:5]
	v_mfma_f32_16x16x32_bf16 v[6:9], v[10:13], v[122:125], 0
	v_mfma_f32_16x16x32_bf16 v[158:161], v[10:13], v[62:65], 0
	v_mfma_f32_16x16x32_bf16 v[166:169], v[10:13], v[94:97], 0
	v_mfma_f32_16x16x32_bf16 v[174:177], v[10:13], v[110:113], 0
	v_mfma_f32_16x16x32_bf16 v[6:9], v[14:17], v[126:129], v[6:9]
	v_mfma_f32_16x16x32_bf16 v[158:161], v[14:17], v[90:93], v[158:161]
	v_mfma_f32_16x16x32_bf16 v[166:169], v[14:17], v[106:109], v[166:169]
	v_mfma_f32_16x16x32_bf16 v[174:177], v[14:17], v[118:121], v[174:177]
	s_setprio 0
	s_setprio 1
	v_mfma_f32_16x16x32_bf16 v[10:13], v[18:21], v[62:65], 0
	v_mfma_f32_16x16x32_bf16 v[178:181], v[22:25], v[90:93], v[10:13]
	v_mfma_f32_16x16x32_bf16 v[10:13], v[26:29], v[62:65], 0
	v_mfma_f32_16x16x32_bf16 v[182:185], v[30:33], v[90:93], v[10:13]
	v_mfma_f32_16x16x32_bf16 v[10:13], v[18:21], v[94:97], 0
	v_mfma_f32_16x16x32_bf16 v[186:189], v[22:25], v[106:109], v[10:13]
	v_mfma_f32_16x16x32_bf16 v[10:13], v[26:29], v[94:97], 0
	v_mfma_f32_16x16x32_bf16 v[190:193], v[30:33], v[106:109], v[10:13]
	v_mfma_f32_16x16x32_bf16 v[10:13], v[18:21], v[110:113], 0
	v_mfma_f32_16x16x32_bf16 v[194:197], v[22:25], v[118:121], v[10:13]
	v_mfma_f32_16x16x32_bf16 v[10:13], v[26:29], v[110:113], 0
	v_mfma_f32_16x16x32_bf16 v[198:201], v[30:33], v[118:121], v[10:13]
	v_mfma_f32_16x16x32_bf16 v[10:13], v[18:21], v[122:125], 0
	v_mfma_f32_16x16x32_bf16 v[202:205], v[22:25], v[126:129], v[10:13]
	v_mfma_f32_16x16x32_bf16 v[10:13], v[26:29], v[122:125], 0
	v_mfma_f32_16x16x32_bf16 v[206:209], v[30:33], v[126:129], v[10:13]
	s_setprio 0
	s_barrier
; template <class Epi, class Sched>
; __device__ __forceinline__ void gemm_phase(PG8_LAS unsigned char* lds, const void* wsbase, const int K, const int ldb, const Sched& S, const Epi& E) {
;     ...
;         PG8_ITER(0, PG8_FIRSTW + 2 + Epi::NVM, PG8_FIRSTW + 6 + Epi::NVM, PG8_FIRSTW + 2 + Epi::NVM, PG8_FIRSTW + 6);
;         for (int t = 2; t < nt; t += 2) PG8_ITER(t, 8 + PG8_SLK1, 8 + PG8_SLK2, 8 + PG8_SLK1, 8 + PG8_SLK2);
	s_nop 4
	ds_read_b128 v[10:13], v144
	ds_read_b128 v[14:17], v144 offset:1024
	ds_read_b128 v[18:21], v144 offset:2048
	ds_read_b128 v[22:25], v144 offset:3072
	ds_read_b128 v[210:213], v145
	ds_read_b128 v[214:217], v145 offset:1024
	ds_read_b128 v[218:221], v145 offset:2048
	ds_read_b128 v[222:225], v145 offset:3072
	s_mov_b32 m0, s56
	ds_read_b128 v[26:29], v143 offset:32768
	ds_read_b128 v[30:33], v143 offset:33792
	ds_read_b128 v[62:65], v143 offset:34816
	ds_read_b128 v[226:229], v143 offset:35840
	ds_read_b128 v[232:235], v143 offset:36864
	ds_read_b128 v[236:239], v143 offset:37888
	ds_read_b128 v[240:243], v143 offset:38912
	ds_read_b128 v[244:247], v143 offset:39936
	buffer_load_dwordx4 v138, s[16:19], s3 offen lds
	s_mov_b32 m0, s57
	s_nop 0
	buffer_load_dwordx4 v140, s[16:19], s3 offen lds
	s_waitcnt vmcnt(26)
	s_waitcnt lgkmcnt(0)
	s_barrier
	s_setprio 1
	s_waitcnt lgkmcnt(7)
	v_mfma_f32_16x16x32_bf16 v[66:69], v[10:13], v[26:29], v[66:69]
	s_waitcnt lgkmcnt(6)
	v_mfma_f32_16x16x32_bf16 v[126:129], v[14:17], v[30:33], v[66:69]
	v_mfma_f32_16x16x32_bf16 v[66:69], v[18:21], v[26:29], v[70:73]
	v_mfma_f32_16x16x32_bf16 v[122:125], v[22:25], v[30:33], v[66:69]
	s_waitcnt lgkmcnt(5)
	v_mfma_f32_16x16x32_bf16 v[66:69], v[10:13], v[62:65], v[74:77]
	s_waitcnt lgkmcnt(4)
	v_mfma_f32_16x16x32_bf16 v[110:113], v[14:17], v[226:229], v[66:69]
	v_mfma_f32_16x16x32_bf16 v[66:69], v[18:21], v[62:65], v[78:81]
	v_mfma_f32_16x16x32_bf16 v[106:109], v[22:25], v[226:229], v[66:69]
	s_waitcnt lgkmcnt(3)
	v_mfma_f32_16x16x32_bf16 v[66:69], v[10:13], v[232:235], v[82:85]
	s_waitcnt lgkmcnt(2)
	v_mfma_f32_16x16x32_bf16 v[94:97], v[14:17], v[236:239], v[66:69]
	v_mfma_f32_16x16x32_bf16 v[66:69], v[18:21], v[232:235], v[86:89]
	v_mfma_f32_16x16x32_bf16 v[90:93], v[22:25], v[236:239], v[66:69]
	s_waitcnt lgkmcnt(1)
	v_mfma_f32_16x16x32_bf16 v[66:69], v[10:13], v[240:243], v[98:101]
	s_waitcnt lgkmcnt(0)
	v_mfma_f32_16x16x32_bf16 v[78:81], v[14:17], v[244:247], v[66:69]
	v_mfma_f32_16x16x32_bf16 v[66:69], v[18:21], v[240:243], v[102:105]
	v_mfma_f32_16x16x32_bf16 v[74:77], v[22:25], v[244:247], v[66:69]
	s_setprio 0
	s_setprio 1
	v_mfma_f32_16x16x32_bf16 v[66:69], v[210:213], v[26:29], v[114:117]
	v_mfma_f32_16x16x32_bf16 v[26:29], v[218:221], v[26:29], v[34:37]
	v_mfma_f32_16x16x32_bf16 v[114:117], v[222:225], v[30:33], v[26:29]
	v_mfma_f32_16x16x32_bf16 v[26:29], v[210:213], v[62:65], v[38:41]
	v_mfma_f32_16x16x32_bf16 v[102:105], v[214:217], v[226:229], v[26:29]
	v_mfma_f32_16x16x32_bf16 v[26:29], v[218:221], v[62:65], v[42:45]
	v_mfma_f32_16x16x32_bf16 v[98:101], v[222:225], v[226:229], v[26:29]
	v_mfma_f32_16x16x32_bf16 v[26:29], v[210:213], v[232:235], v[46:49]
	v_mfma_f32_16x16x32_bf16 v[86:89], v[214:217], v[236:239], v[26:29]
	v_mfma_f32_16x16x32_bf16 v[26:29], v[218:221], v[232:235], v[50:53]
	v_mfma_f32_16x16x32_bf16 v[82:85], v[222:225], v[236:239], v[26:29]
	v_mfma_f32_16x16x32_bf16 v[26:29], v[210:213], v[240:243], v[54:57]
	v_mfma_f32_16x16x32_bf16 v[70:73], v[214:217], v[244:247], v[26:29]
	v_mfma_f32_16x16x32_bf16 v[26:29], v[218:221], v[240:243], v[58:61]
	v_mfma_f32_16x16x32_bf16 v[118:121], v[214:217], v[30:33], v[66:69]
	v_mfma_f32_16x16x32_bf16 v[66:69], v[222:225], v[244:247], v[26:29]
	s_setprio 0
	s_barrier
	s_mov_b32 m0, s59
	s_add_i32 s3, s12, 0x180
	ds_read_b128 v[34:37], v143 offset:49152
	ds_read_b128 v[38:41], v143 offset:50176
	ds_read_b128 v[226:229], v143 offset:51200
	ds_read_b128 v[232:235], v143 offset:52224
	ds_read_b128 v[236:239], v143 offset:53248
	ds_read_b128 v[240:243], v143 offset:54272
	ds_read_b128 v[244:247], v143 offset:55296
	ds_read_b128 v[248:251], v143 offset:56320
	buffer_load_dwordx4 v1, s[16:19], s3 offen lds
	s_mov_b32 m0, s60
	s_nop 0
	buffer_load_dwordx4 v136, s[16:19], s3 offen lds
	s_add_i32 s3, s12, 0x100180
	s_mov_b32 m0, s63
	s_nop 0
	buffer_load_dwordx4 v1, s[16:19], s3 offen lds
	s_mov_b32 m0, s64
	s_nop 0
	buffer_load_dwordx4 v136, s[16:19], s3 offen lds
	s_mov_b32 m0, s61
	s_nop 0
	buffer_load_dwordx4 v137, s[16:19], s2 offen lds
	s_mov_b32 m0, s62
	s_nop 0
	buffer_load_dwordx4 v139, s[16:19], s2 offen lds
	s_waitcnt vmcnt(14)
	s_waitcnt lgkmcnt(0)
	s_barrier
	s_setprio 1
	s_waitcnt lgkmcnt(7)
	v_mfma_f32_16x16x32_bf16 v[26:29], v[10:13], v[34:37], v[154:157]
	s_waitcnt lgkmcnt(6)
	v_mfma_f32_16x16x32_bf16 v[62:65], v[14:17], v[38:41], v[26:29]
	v_mfma_f32_16x16x32_bf16 v[26:29], v[18:21], v[34:37], v[158:161]
	v_mfma_f32_16x16x32_bf16 v[58:61], v[22:25], v[38:41], v[26:29]
	s_waitcnt lgkmcnt(5)
	v_mfma_f32_16x16x32_bf16 v[26:29], v[10:13], v[226:229], v[162:165]
	s_waitcnt lgkmcnt(4)
	v_mfma_f32_16x16x32_bf16 v[46:49], v[14:17], v[232:235], v[26:29]
	v_mfma_f32_16x16x32_bf16 v[26:29], v[18:21], v[226:229], v[166:169]
	v_mfma_f32_16x16x32_bf16 v[42:45], v[22:25], v[232:235], v[26:29]
	s_waitcnt lgkmcnt(3)
	v_mfma_f32_16x16x32_bf16 v[26:29], v[10:13], v[236:239], v[170:173]
	s_waitcnt lgkmcnt(1)
	v_mfma_f32_16x16x32_bf16 v[2:5], v[10:13], v[244:247], v[2:5]
	v_mfma_f32_16x16x32_bf16 v[30:33], v[14:17], v[240:243], v[26:29]
	v_mfma_f32_16x16x32_bf16 v[26:29], v[18:21], v[236:239], v[174:177]
	s_waitcnt lgkmcnt(0)
	v_mfma_f32_16x16x32_bf16 v[14:17], v[14:17], v[248:251], v[2:5]
	v_mfma_f32_16x16x32_bf16 v[2:5], v[18:21], v[244:247], v[6:9]
	v_mfma_f32_16x16x32_bf16 v[26:29], v[22:25], v[240:243], v[26:29]
	v_mfma_f32_16x16x32_bf16 v[10:13], v[22:25], v[248:251], v[2:5]
	s_setprio 0
	s_setprio 1
	v_mfma_f32_16x16x32_bf16 v[2:5], v[210:213], v[34:37], v[178:181]
	v_mfma_f32_16x16x32_bf16 v[54:57], v[214:217], v[38:41], v[2:5]
	v_mfma_f32_16x16x32_bf16 v[2:5], v[218:221], v[34:37], v[182:185]
	v_mfma_f32_16x16x32_bf16 v[50:53], v[222:225], v[38:41], v[2:5]
	v_mfma_f32_16x16x32_bf16 v[2:5], v[210:213], v[226:229], v[186:189]
	v_mfma_f32_16x16x32_bf16 v[38:41], v[214:217], v[232:235], v[2:5]
	v_mfma_f32_16x16x32_bf16 v[2:5], v[218:221], v[226:229], v[190:193]
	v_mfma_f32_16x16x32_bf16 v[34:37], v[222:225], v[232:235], v[2:5]
	v_mfma_f32_16x16x32_bf16 v[2:5], v[210:213], v[236:239], v[194:197]
	v_mfma_f32_16x16x32_bf16 v[22:25], v[214:217], v[240:243], v[2:5]
	v_mfma_f32_16x16x32_bf16 v[2:5], v[218:221], v[236:239], v[198:201]
	v_mfma_f32_16x16x32_bf16 v[18:21], v[222:225], v[240:243], v[2:5]
	v_mfma_f32_16x16x32_bf16 v[2:5], v[210:213], v[244:247], v[202:205]
	v_mfma_f32_16x16x32_bf16 v[6:9], v[214:217], v[248:251], v[2:5]
	v_mfma_f32_16x16x32_bf16 v[2:5], v[218:221], v[244:247], v[206:209]
	v_mfma_f32_16x16x32_bf16 v[2:5], v[222:225], v[248:251], v[2:5]
	s_setprio 0
	s_barrier
	s_add_i32 s2, s12, 0x200
	s_addk_i32 s1, 0x200
	s_mov_b32 s3, 0
	.p2alignl 6, 3212836864

.LBB0_506:
	ds_read_b128 v[2:5], v139
	ds_read_b128 v[6:9], v139 offset:1024
	ds_read_b128 v[10:13], v139 offset:2048
	ds_read_b128 v[14:17], v139 offset:3072
	ds_read_b128 v[18:21], v140
	ds_read_b128 v[22:25], v140 offset:1024
	ds_read_b128 v[26:29], v140 offset:2048
	ds_read_b128 v[30:33], v140 offset:3072
	s_add_i32 s15, s60, 0x100
	s_add_i32 s14, s60, 0x180
	s_add_i32 s30, s61, 0x100
	s_add_i32 s31, s60, 0x80
	s_mov_b32 s16, s12
	s_mov_b32 m0, s54
	ds_read_b128 v[34:37], v141
	ds_read_b128 v[38:41], v141 offset:1024
	ds_read_b128 v[42:45], v141 offset:2048
	ds_read_b128 v[46:49], v141 offset:3072
	ds_read_b128 v[50:53], v141 offset:4096
	ds_read_b128 v[54:57], v141 offset:5120
	ds_read_b128 v[58:61], v141 offset:6144
	ds_read_b128 v[62:65], v141 offset:7168
	buffer_load_dwordx4 v136, s[16:19], s31 offen lds
	s_mov_b32 m0, s55
	s_nop 0
	buffer_load_dwordx4 v138, s[16:19], s31 offen lds
	s_waitcnt vmcnt(26)
	s_waitcnt lgkmcnt(0)
	s_barrier
	s_setprio 1
	s_waitcnt lgkmcnt(0)
	v_mfma_f32_16x16x32_bf16 v[90:93], v[2:5], v[58:61], 0
	v_mfma_f32_16x16x32_bf16 v[66:69], v[2:5], v[34:37], 0
	v_mfma_f32_16x16x32_bf16 v[70:73], v[10:13], v[34:37], 0
	v_mfma_f32_16x16x32_bf16 v[74:77], v[2:5], v[42:45], 0
	v_mfma_f32_16x16x32_bf16 v[78:81], v[10:13], v[42:45], 0
	v_mfma_f32_16x16x32_bf16 v[82:85], v[2:5], v[50:53], 0
	v_mfma_f32_16x16x32_bf16 v[86:89], v[10:13], v[50:53], 0
	v_mfma_f32_16x16x32_bf16 v[94:97], v[6:9], v[62:65], v[90:93]
	v_mfma_f32_16x16x32_bf16 v[90:93], v[10:13], v[58:61], 0
	v_mfma_f32_16x16x32_bf16 v[66:69], v[6:9], v[38:41], v[66:69]
	v_mfma_f32_16x16x32_bf16 v[70:73], v[14:17], v[38:41], v[70:73]
	v_mfma_f32_16x16x32_bf16 v[74:77], v[6:9], v[46:49], v[74:77]
	v_mfma_f32_16x16x32_bf16 v[78:81], v[14:17], v[46:49], v[78:81]
	v_mfma_f32_16x16x32_bf16 v[82:85], v[6:9], v[54:57], v[82:85]
	v_mfma_f32_16x16x32_bf16 v[86:89], v[14:17], v[54:57], v[86:89]
	v_mfma_f32_16x16x32_bf16 v[102:105], v[14:17], v[62:65], v[90:93]
	s_setprio 0
	s_setprio 1
	v_mfma_f32_16x16x32_bf16 v[90:93], v[18:21], v[34:37], 0
	v_mfma_f32_16x16x32_bf16 v[34:37], v[26:29], v[34:37], 0
	v_mfma_f32_16x16x32_bf16 v[110:113], v[22:25], v[38:41], v[90:93]
	v_mfma_f32_16x16x32_bf16 v[34:37], v[30:33], v[38:41], v[34:37]
	v_mfma_f32_16x16x32_bf16 v[38:41], v[18:21], v[42:45], 0
	v_mfma_f32_16x16x32_bf16 v[42:45], v[26:29], v[42:45], 0
	v_mfma_f32_16x16x32_bf16 v[38:41], v[22:25], v[46:49], v[38:41]
	v_mfma_f32_16x16x32_bf16 v[42:45], v[30:33], v[46:49], v[42:45]
	v_mfma_f32_16x16x32_bf16 v[46:49], v[18:21], v[50:53], 0
	v_mfma_f32_16x16x32_bf16 v[50:53], v[26:29], v[50:53], 0
	v_mfma_f32_16x16x32_bf16 v[46:49], v[22:25], v[54:57], v[46:49]
	v_mfma_f32_16x16x32_bf16 v[54:57], v[30:33], v[54:57], v[50:53]
	v_mfma_f32_16x16x32_bf16 v[50:53], v[18:21], v[58:61], 0
	v_mfma_f32_16x16x32_bf16 v[144:147], v[22:25], v[62:65], v[50:53]
	v_mfma_f32_16x16x32_bf16 v[50:53], v[26:29], v[58:61], 0
	v_mfma_f32_16x16x32_bf16 v[148:151], v[30:33], v[62:65], v[50:53]
	s_setprio 0
	s_barrier
	s_mov_b32 m0, s39
	s_nop 3
	ds_read_b128 v[50:53], v141 offset:16384
	ds_read_b128 v[58:61], v141 offset:17408
	ds_read_b128 v[62:65], v141 offset:18432
	ds_read_b128 v[90:93], v141 offset:19456
	ds_read_b128 v[98:101], v141 offset:20480
	ds_read_b128 v[106:109], v141 offset:21504
	ds_read_b128 v[114:117], v141 offset:22528
	ds_read_b128 v[118:121], v141 offset:23552
	buffer_load_dwordx4 v1, s[16:19], s30 offen lds
	s_mov_b32 m0, s40
	s_nop 0
	buffer_load_dwordx4 v134, s[16:19], s30 offen lds
	s_add_i32 s30, s61, 0x18100
	s_mov_b32 m0, s41
	s_nop 0
	buffer_load_dwordx4 v1, s[16:19], s30 offen lds
	s_mov_b32 m0, s42
	s_nop 0
	buffer_load_dwordx4 v134, s[16:19], s30 offen lds
	s_mov_b32 m0, s38
	s_nop 0
	buffer_load_dwordx4 v135, s[16:19], s15 offen lds
	s_mov_b32 m0, s43
	s_nop 0
	buffer_load_dwordx4 v137, s[16:19], s15 offen lds
	s_waitcnt vmcnt(30)
	s_waitcnt lgkmcnt(0)
	s_barrier
	s_setprio 1
	s_waitcnt lgkmcnt(0)
	v_mfma_f32_16x16x32_bf16 v[122:125], v[2:5], v[50:53], 0
	v_mfma_f32_16x16x32_bf16 v[152:155], v[6:9], v[58:61], v[122:125]
	v_mfma_f32_16x16x32_bf16 v[122:125], v[10:13], v[50:53], 0
	v_mfma_f32_16x16x32_bf16 v[156:159], v[14:17], v[58:61], v[122:125]
	v_mfma_f32_16x16x32_bf16 v[122:125], v[2:5], v[62:65], 0
	v_mfma_f32_16x16x32_bf16 v[160:163], v[6:9], v[90:93], v[122:125]
	v_mfma_f32_16x16x32_bf16 v[122:125], v[10:13], v[62:65], 0
	v_mfma_f32_16x16x32_bf16 v[164:167], v[14:17], v[90:93], v[122:125]
	v_mfma_f32_16x16x32_bf16 v[122:125], v[2:5], v[98:101], 0
	v_mfma_f32_16x16x32_bf16 v[2:5], v[2:5], v[114:117], 0
	v_mfma_f32_16x16x32_bf16 v[168:171], v[6:9], v[106:109], v[122:125]
	v_mfma_f32_16x16x32_bf16 v[2:5], v[6:9], v[118:121], v[2:5]
	v_mfma_f32_16x16x32_bf16 v[6:9], v[10:13], v[114:117], 0
	v_mfma_f32_16x16x32_bf16 v[122:125], v[10:13], v[98:101], 0
	v_mfma_f32_16x16x32_bf16 v[6:9], v[14:17], v[118:121], v[6:9]
	v_mfma_f32_16x16x32_bf16 v[172:175], v[14:17], v[106:109], v[122:125]
	s_setprio 0
	s_setprio 1
	v_mfma_f32_16x16x32_bf16 v[10:13], v[18:21], v[50:53], 0
	v_mfma_f32_16x16x32_bf16 v[14:17], v[22:25], v[58:61], v[10:13]
	v_mfma_f32_16x16x32_bf16 v[10:13], v[26:29], v[50:53], 0
	v_mfma_f32_16x16x32_bf16 v[176:179], v[30:33], v[58:61], v[10:13]
	v_mfma_f32_16x16x32_bf16 v[10:13], v[18:21], v[62:65], 0
	v_mfma_f32_16x16x32_bf16 v[180:183], v[22:25], v[90:93], v[10:13]
	v_mfma_f32_16x16x32_bf16 v[10:13], v[26:29], v[62:65], 0
	v_mfma_f32_16x16x32_bf16 v[184:187], v[30:33], v[90:93], v[10:13]
	v_mfma_f32_16x16x32_bf16 v[10:13], v[18:21], v[98:101], 0
	v_mfma_f32_16x16x32_bf16 v[188:191], v[22:25], v[106:109], v[10:13]
	v_mfma_f32_16x16x32_bf16 v[10:13], v[26:29], v[98:101], 0
	v_mfma_f32_16x16x32_bf16 v[192:195], v[30:33], v[106:109], v[10:13]
	v_mfma_f32_16x16x32_bf16 v[10:13], v[18:21], v[114:117], 0
	v_mfma_f32_16x16x32_bf16 v[196:199], v[22:25], v[118:121], v[10:13]
	v_mfma_f32_16x16x32_bf16 v[10:13], v[26:29], v[114:117], 0
	v_mfma_f32_16x16x32_bf16 v[200:203], v[30:33], v[118:121], v[10:13]
	s_setprio 0
	s_barrier
; template <class Epi, class Sched>
; __device__ __forceinline__ void gemm_phase(PG8_LAS unsigned char* lds, const void* wsbase, const int K, const int ldb, const Sched& S, const Epi& E) {
;     ...
;         PG8_ITER(0, PG8_FIRSTW + 2 + Epi::NVM, PG8_FIRSTW + 6 + Epi::NVM, PG8_FIRSTW + 2 + Epi::NVM, PG8_FIRSTW + 6);
;         for (int t = 2; t < nt; t += 2) PG8_ITER(t, 8 + PG8_SLK1, 8 + PG8_SLK2, 8 + PG8_SLK1, 8 + PG8_SLK2);
	s_nop 4
	ds_read_b128 v[10:13], v142
	ds_read_b128 v[22:25], v142 offset:1024
	ds_read_b128 v[30:33], v142 offset:2048
	ds_read_b128 v[204:207], v142 offset:3072
	ds_read_b128 v[208:211], v143
	ds_read_b128 v[212:215], v143 offset:1024
	ds_read_b128 v[216:219], v143 offset:2048
	ds_read_b128 v[220:223], v143 offset:3072
	s_mov_b32 m0, s44
	ds_read_b128 v[18:21], v141 offset:32768
	ds_read_b128 v[26:29], v141 offset:33792
	ds_read_b128 v[62:65], v141 offset:34816
	ds_read_b128 v[224:227], v141 offset:35840
	ds_read_b128 v[232:235], v141 offset:36864
	ds_read_b128 v[236:239], v141 offset:37888
	ds_read_b128 v[240:243], v141 offset:38912
	ds_read_b128 v[244:247], v141 offset:39936
	buffer_load_dwordx4 v136, s[16:19], s15 offen lds
	s_mov_b32 m0, s45
	s_nop 0
	buffer_load_dwordx4 v138, s[16:19], s15 offen lds
	s_waitcnt vmcnt(26)
	s_waitcnt lgkmcnt(0)
	s_barrier
	s_setprio 1
	s_waitcnt lgkmcnt(0)
	v_mfma_f32_16x16x32_bf16 v[50:53], v[10:13], v[18:21], v[66:69]
	v_mfma_f32_16x16x32_bf16 v[126:129], v[22:25], v[26:29], v[50:53]
	v_mfma_f32_16x16x32_bf16 v[50:53], v[30:33], v[18:21], v[70:73]
	v_mfma_f32_16x16x32_bf16 v[118:121], v[204:207], v[26:29], v[50:53]
	v_mfma_f32_16x16x32_bf16 v[50:53], v[10:13], v[62:65], v[74:77]
	v_mfma_f32_16x16x32_bf16 v[106:109], v[22:25], v[224:227], v[50:53]
	v_mfma_f32_16x16x32_bf16 v[50:53], v[30:33], v[62:65], v[78:81]
	v_mfma_f32_16x16x32_bf16 v[98:101], v[204:207], v[224:227], v[50:53]
	v_mfma_f32_16x16x32_bf16 v[50:53], v[10:13], v[232:235], v[82:85]
	v_mfma_f32_16x16x32_bf16 v[90:93], v[22:25], v[236:239], v[50:53]
	v_mfma_f32_16x16x32_bf16 v[50:53], v[30:33], v[232:235], v[86:89]
	v_mfma_f32_16x16x32_bf16 v[82:85], v[204:207], v[236:239], v[50:53]
	v_mfma_f32_16x16x32_bf16 v[50:53], v[10:13], v[240:243], v[94:97]
	v_mfma_f32_16x16x32_bf16 v[58:61], v[22:25], v[244:247], v[50:53]
	v_mfma_f32_16x16x32_bf16 v[50:53], v[30:33], v[240:243], v[102:105]
	v_mfma_f32_16x16x32_bf16 v[50:53], v[204:207], v[244:247], v[50:53]
	s_setprio 0
	s_setprio 1
	v_mfma_f32_16x16x32_bf16 v[66:69], v[208:211], v[18:21], v[110:113]
	v_mfma_f32_16x16x32_bf16 v[18:21], v[216:219], v[18:21], v[34:37]
	v_mfma_f32_16x16x32_bf16 v[114:117], v[220:223], v[26:29], v[18:21]
	v_mfma_f32_16x16x32_bf16 v[18:21], v[208:211], v[62:65], v[38:41]
	v_mfma_f32_16x16x32_bf16 v[110:113], v[212:215], v[224:227], v[18:21]
	v_mfma_f32_16x16x32_bf16 v[18:21], v[216:219], v[62:65], v[42:45]
	v_mfma_f32_16x16x32_bf16 v[102:105], v[220:223], v[224:227], v[18:21]
	v_mfma_f32_16x16x32_bf16 v[18:21], v[208:211], v[232:235], v[46:49]
	v_mfma_f32_16x16x32_bf16 v[94:97], v[212:215], v[236:239], v[18:21]
	v_mfma_f32_16x16x32_bf16 v[18:21], v[216:219], v[232:235], v[54:57]
	v_mfma_f32_16x16x32_bf16 v[86:89], v[220:223], v[236:239], v[18:21]
	v_mfma_f32_16x16x32_bf16 v[18:21], v[208:211], v[240:243], v[144:147]
	v_mfma_f32_16x16x32_bf16 v[62:65], v[212:215], v[244:247], v[18:21]
	v_mfma_f32_16x16x32_bf16 v[18:21], v[216:219], v[240:243], v[148:151]
	v_mfma_f32_16x16x32_bf16 v[122:125], v[212:215], v[26:29], v[66:69]
	v_mfma_f32_16x16x32_bf16 v[54:57], v[220:223], v[244:247], v[18:21]
	s_setprio 0
	s_barrier
	s_mov_b32 m0, s47
	s_add_i32 s15, s61, 0x180
	ds_read_b128 v[38:41], v141 offset:49152
	ds_read_b128 v[46:49], v141 offset:50176
	ds_read_b128 v[144:147], v141 offset:51200
	ds_read_b128 v[148:151], v141 offset:52224
	ds_read_b128 v[224:227], v141 offset:53248
	ds_read_b128 v[232:235], v141 offset:54272
	ds_read_b128 v[236:239], v141 offset:55296
	ds_read_b128 v[240:243], v141 offset:56320
	buffer_load_dwordx4 v1, s[16:19], s15 offen lds
	s_mov_b32 m0, s48
	s_nop 0
	buffer_load_dwordx4 v134, s[16:19], s15 offen lds
	s_add_i32 s15, s61, 0x18180
	s_mov_b32 m0, s51
	s_nop 0
	buffer_load_dwordx4 v1, s[16:19], s15 offen lds
	s_mov_b32 m0, s52
	s_nop 0
	buffer_load_dwordx4 v134, s[16:19], s15 offen lds
	s_mov_b32 m0, s49
	s_nop 0
	buffer_load_dwordx4 v135, s[16:19], s14 offen lds
	s_mov_b32 m0, s50
	s_nop 0
	buffer_load_dwordx4 v137, s[16:19], s14 offen lds
	s_waitcnt vmcnt(14)
	s_waitcnt lgkmcnt(0)
	s_barrier
	s_setprio 1
	s_waitcnt lgkmcnt(0)
	v_mfma_f32_16x16x32_bf16 v[18:21], v[10:13], v[38:41], v[152:155]
	v_mfma_f32_16x16x32_bf16 v[74:77], v[22:25], v[46:49], v[18:21]
	v_mfma_f32_16x16x32_bf16 v[18:21], v[30:33], v[38:41], v[156:159]
	v_mfma_f32_16x16x32_bf16 v[66:69], v[204:207], v[46:49], v[18:21]
	v_mfma_f32_16x16x32_bf16 v[18:21], v[10:13], v[144:147], v[160:163]
	v_mfma_f32_16x16x32_bf16 v[42:45], v[22:25], v[148:151], v[18:21]
	v_mfma_f32_16x16x32_bf16 v[18:21], v[30:33], v[144:147], v[164:167]
	v_mfma_f32_16x16x32_bf16 v[34:37], v[204:207], v[148:151], v[18:21]
	v_mfma_f32_16x16x32_bf16 v[18:21], v[10:13], v[224:227], v[168:171]
	v_mfma_f32_16x16x32_bf16 v[2:5], v[10:13], v[236:239], v[2:5]
	v_mfma_f32_16x16x32_bf16 v[26:29], v[22:25], v[232:235], v[18:21]
	v_mfma_f32_16x16x32_bf16 v[18:21], v[30:33], v[224:227], v[172:175]
	v_mfma_f32_16x16x32_bf16 v[10:13], v[22:25], v[240:243], v[2:5]
	v_mfma_f32_16x16x32_bf16 v[2:5], v[30:33], v[236:239], v[6:9]
	v_mfma_f32_16x16x32_bf16 v[18:21], v[204:207], v[232:235], v[18:21]
	v_mfma_f32_16x16x32_bf16 v[2:5], v[204:207], v[240:243], v[2:5]
	s_setprio 0
	s_setprio 1
	v_mfma_f32_16x16x32_bf16 v[6:9], v[208:211], v[38:41], v[14:17]
	v_mfma_f32_16x16x32_bf16 v[78:81], v[212:215], v[46:49], v[6:9]
	v_mfma_f32_16x16x32_bf16 v[6:9], v[216:219], v[38:41], v[176:179]
	v_mfma_f32_16x16x32_bf16 v[70:73], v[220:223], v[46:49], v[6:9]
	v_mfma_f32_16x16x32_bf16 v[6:9], v[208:211], v[144:147], v[180:183]
	v_mfma_f32_16x16x32_bf16 v[46:49], v[212:215], v[148:151], v[6:9]
	v_mfma_f32_16x16x32_bf16 v[6:9], v[216:219], v[144:147], v[184:187]
	v_mfma_f32_16x16x32_bf16 v[38:41], v[220:223], v[148:151], v[6:9]
	v_mfma_f32_16x16x32_bf16 v[6:9], v[208:211], v[224:227], v[188:191]
	v_mfma_f32_16x16x32_bf16 v[30:33], v[212:215], v[232:235], v[6:9]
	v_mfma_f32_16x16x32_bf16 v[6:9], v[216:219], v[224:227], v[192:195]
	v_mfma_f32_16x16x32_bf16 v[22:25], v[220:223], v[232:235], v[6:9]
	v_mfma_f32_16x16x32_bf16 v[6:9], v[208:211], v[236:239], v[196:199]
	v_mfma_f32_16x16x32_bf16 v[14:17], v[212:215], v[240:243], v[6:9]
	v_mfma_f32_16x16x32_bf16 v[6:9], v[216:219], v[236:239], v[200:203]
	v_mfma_f32_16x16x32_bf16 v[6:9], v[220:223], v[240:243], v[6:9]
	s_setprio 0
	s_barrier
	s_add_i32 s14, s61, 0x200
	s_add_i32 s15, s60, 0x200
	s_mov_b32 s60, 0
	.p2alignl 6, 3212836864

.LBB0_781:
	ds_read_b128 v[2:5], v132
	ds_read_b128 v[6:9], v132 offset:1024
	ds_read_b128 v[10:13], v132 offset:2048
	ds_read_b128 v[14:17], v132 offset:3072
	ds_read_b128 v[18:21], v133
	ds_read_b128 v[22:25], v133 offset:1024
	ds_read_b128 v[26:29], v133 offset:2048
	ds_read_b128 v[30:33], v133 offset:3072
	s_add_i32 s17, s60, 0x100
	s_mov_b32 m0, s51
	ds_read_b128 v[34:37], v134
	ds_read_b128 v[38:41], v134 offset:1024
	ds_read_b128 v[42:45], v134 offset:2048
	ds_read_b128 v[46:49], v134 offset:3072
	ds_read_b128 v[50:53], v134 offset:4096
	ds_read_b128 v[54:57], v134 offset:5120
	ds_read_b128 v[58:61], v134 offset:6144
	ds_read_b128 v[62:65], v134 offset:7168
	buffer_load_dwordx4 v141, s[12:15], s47 offen lds
	s_mov_b32 m0, s52
	s_nop 0
	buffer_load_dwordx4 v143, s[12:15], s47 offen lds
	s_waitcnt vmcnt(18)
	s_waitcnt lgkmcnt(0)
	s_barrier
	s_setprio 1
	s_waitcnt lgkmcnt(1)
	v_mfma_f32_16x16x32_bf16 v[90:93], v[2:5], v[58:61], 0
	v_mfma_f32_16x16x32_bf16 v[66:69], v[2:5], v[34:37], 0
	v_mfma_f32_16x16x32_bf16 v[70:73], v[10:13], v[34:37], 0
	v_mfma_f32_16x16x32_bf16 v[74:77], v[2:5], v[42:45], 0
	v_mfma_f32_16x16x32_bf16 v[78:81], v[10:13], v[42:45], 0
	v_mfma_f32_16x16x32_bf16 v[82:85], v[2:5], v[50:53], 0
	v_mfma_f32_16x16x32_bf16 v[86:89], v[10:13], v[50:53], 0
	s_waitcnt lgkmcnt(0)
	v_mfma_f32_16x16x32_bf16 v[94:97], v[6:9], v[62:65], v[90:93]
	v_mfma_f32_16x16x32_bf16 v[90:93], v[10:13], v[58:61], 0
	v_mfma_f32_16x16x32_bf16 v[66:69], v[6:9], v[38:41], v[66:69]
	v_mfma_f32_16x16x32_bf16 v[70:73], v[14:17], v[38:41], v[70:73]
	v_mfma_f32_16x16x32_bf16 v[74:77], v[6:9], v[46:49], v[74:77]
	v_mfma_f32_16x16x32_bf16 v[78:81], v[14:17], v[46:49], v[78:81]
	v_mfma_f32_16x16x32_bf16 v[82:85], v[6:9], v[54:57], v[82:85]
	v_mfma_f32_16x16x32_bf16 v[86:89], v[14:17], v[54:57], v[86:89]
	v_mfma_f32_16x16x32_bf16 v[102:105], v[14:17], v[62:65], v[90:93]
	s_setprio 0
	s_setprio 1
	v_mfma_f32_16x16x32_bf16 v[90:93], v[18:21], v[34:37], 0
	v_mfma_f32_16x16x32_bf16 v[34:37], v[26:29], v[34:37], 0
	v_mfma_f32_16x16x32_bf16 v[110:113], v[22:25], v[38:41], v[90:93]
	v_mfma_f32_16x16x32_bf16 v[34:37], v[30:33], v[38:41], v[34:37]
	v_mfma_f32_16x16x32_bf16 v[38:41], v[18:21], v[42:45], 0
	v_mfma_f32_16x16x32_bf16 v[42:45], v[26:29], v[42:45], 0
	v_mfma_f32_16x16x32_bf16 v[38:41], v[22:25], v[46:49], v[38:41]
	v_mfma_f32_16x16x32_bf16 v[42:45], v[30:33], v[46:49], v[42:45]
	v_mfma_f32_16x16x32_bf16 v[46:49], v[18:21], v[50:53], 0
	v_mfma_f32_16x16x32_bf16 v[50:53], v[26:29], v[50:53], 0
	v_mfma_f32_16x16x32_bf16 v[46:49], v[22:25], v[54:57], v[46:49]
	v_mfma_f32_16x16x32_bf16 v[50:53], v[30:33], v[54:57], v[50:53]
	v_mfma_f32_16x16x32_bf16 v[54:57], v[18:21], v[58:61], 0
	v_mfma_f32_16x16x32_bf16 v[58:61], v[26:29], v[58:61], 0
	v_mfma_f32_16x16x32_bf16 v[54:57], v[22:25], v[62:65], v[54:57]
	v_mfma_f32_16x16x32_bf16 v[62:65], v[30:33], v[62:65], v[58:61]
	s_setprio 0
	s_barrier
	s_mov_b32 m0, s19
	s_nop 2
	ds_read_b128 v[58:61], v134 offset:16384
	ds_read_b128 v[90:93], v134 offset:17408
	ds_read_b128 v[98:101], v134 offset:18432
	ds_read_b128 v[106:109], v134 offset:19456
	ds_read_b128 v[114:117], v134 offset:20480
	ds_read_b128 v[118:121], v134 offset:21504
	ds_read_b128 v[122:125], v134 offset:22528
	ds_read_b128 v[126:129], v134 offset:23552
	buffer_load_dwordx4 v130, s[12:15], s17 offen lds
	s_mov_b32 m0, s20
	s_nop 0
	buffer_load_dwordx4 v131, s[12:15], s17 offen lds
	s_add_i32 s17, s60, 0x40100
	s_mov_b32 m0, s21
	s_nop 0
	buffer_load_dwordx4 v130, s[12:15], s17 offen lds
	s_mov_b32 m0, s23
	s_nop 0
	buffer_load_dwordx4 v131, s[12:15], s17 offen lds
	s_mov_b32 m0, s18
	s_nop 0
	buffer_load_dwordx4 v142, s[12:15], s53 offen lds
	s_mov_b32 m0, s40
	s_nop 0
	buffer_load_dwordx4 v144, s[12:15], s53 offen lds
	s_waitcnt vmcnt(22)
	s_waitcnt lgkmcnt(0)
	s_barrier
	s_setprio 1
	s_waitcnt lgkmcnt(7)
	v_mfma_f32_16x16x32_bf16 v[146:149], v[2:5], v[58:61], 0
	s_waitcnt lgkmcnt(5)
	v_mfma_f32_16x16x32_bf16 v[154:157], v[2:5], v[98:101], 0
	s_waitcnt lgkmcnt(3)
	v_mfma_f32_16x16x32_bf16 v[162:165], v[2:5], v[114:117], 0
	s_waitcnt lgkmcnt(1)
	v_mfma_f32_16x16x32_bf16 v[2:5], v[2:5], v[122:125], 0
	v_mfma_f32_16x16x32_bf16 v[146:149], v[6:9], v[90:93], v[146:149]
	v_mfma_f32_16x16x32_bf16 v[154:157], v[6:9], v[106:109], v[154:157]
	v_mfma_f32_16x16x32_bf16 v[162:165], v[6:9], v[118:121], v[162:165]
	s_waitcnt lgkmcnt(0)
	v_mfma_f32_16x16x32_bf16 v[2:5], v[6:9], v[126:129], v[2:5]
	v_mfma_f32_16x16x32_bf16 v[6:9], v[10:13], v[122:125], 0
	v_mfma_f32_16x16x32_bf16 v[150:153], v[10:13], v[58:61], 0
	v_mfma_f32_16x16x32_bf16 v[158:161], v[10:13], v[98:101], 0
	v_mfma_f32_16x16x32_bf16 v[166:169], v[10:13], v[114:117], 0
	v_mfma_f32_16x16x32_bf16 v[6:9], v[14:17], v[126:129], v[6:9]
	v_mfma_f32_16x16x32_bf16 v[150:153], v[14:17], v[90:93], v[150:153]
	v_mfma_f32_16x16x32_bf16 v[158:161], v[14:17], v[106:109], v[158:161]
	v_mfma_f32_16x16x32_bf16 v[166:169], v[14:17], v[118:121], v[166:169]
	s_setprio 0
	s_setprio 1
	v_mfma_f32_16x16x32_bf16 v[10:13], v[18:21], v[58:61], 0
	v_mfma_f32_16x16x32_bf16 v[14:17], v[22:25], v[90:93], v[10:13]
	v_mfma_f32_16x16x32_bf16 v[10:13], v[26:29], v[58:61], 0
	v_mfma_f32_16x16x32_bf16 v[170:173], v[30:33], v[90:93], v[10:13]
	v_mfma_f32_16x16x32_bf16 v[10:13], v[18:21], v[98:101], 0
	v_mfma_f32_16x16x32_bf16 v[174:177], v[22:25], v[106:109], v[10:13]
	v_mfma_f32_16x16x32_bf16 v[10:13], v[26:29], v[98:101], 0
	v_mfma_f32_16x16x32_bf16 v[178:181], v[30:33], v[106:109], v[10:13]
	v_mfma_f32_16x16x32_bf16 v[10:13], v[18:21], v[114:117], 0
	v_mfma_f32_16x16x32_bf16 v[182:185], v[22:25], v[118:121], v[10:13]
	v_mfma_f32_16x16x32_bf16 v[10:13], v[26:29], v[114:117], 0
	v_mfma_f32_16x16x32_bf16 v[186:189], v[30:33], v[118:121], v[10:13]
	v_mfma_f32_16x16x32_bf16 v[10:13], v[18:21], v[122:125], 0
	v_mfma_f32_16x16x32_bf16 v[190:193], v[22:25], v[126:129], v[10:13]
	v_mfma_f32_16x16x32_bf16 v[10:13], v[26:29], v[122:125], 0
	v_mfma_f32_16x16x32_bf16 v[194:197], v[30:33], v[126:129], v[10:13]
	s_setprio 0
	s_barrier
; template <class Epi, class Sched>
; __device__ __forceinline__ void gemm_phase(PG8_LAS unsigned char* lds, const void* wsbase, const int K, const int ldb, const Sched& S, const Epi& E) {
;     ...
;         PG8_ITER(0, PG8_FIRSTW + 2 + Epi::NVM, PG8_FIRSTW + 6 + Epi::NVM, PG8_FIRSTW + 2 + Epi::NVM, PG8_FIRSTW + 6);
;         for (int t = 2; t < nt; t += 2) PG8_ITER(t, 8 + PG8_SLK1, 8 + PG8_SLK2, 8 + PG8_SLK1, 8 + PG8_SLK2);
	s_nop 4
	ds_read_b128 v[10:13], v135
	ds_read_b128 v[22:25], v135 offset:1024
	ds_read_b128 v[30:33], v135 offset:2048
	ds_read_b128 v[198:201], v135 offset:3072
	ds_read_b128 v[202:205], v136
	ds_read_b128 v[206:209], v136 offset:1024
	ds_read_b128 v[210:213], v136 offset:2048
	ds_read_b128 v[214:217], v136 offset:3072
	s_mov_b32 m0, s41
	ds_read_b128 v[18:21], v134 offset:32768
	ds_read_b128 v[26:29], v134 offset:33792
	ds_read_b128 v[218:221], v134 offset:34816
	ds_read_b128 v[222:225], v134 offset:35840
	ds_read_b128 v[226:229], v134 offset:36864
	ds_read_b128 v[232:235], v134 offset:37888
	ds_read_b128 v[236:239], v134 offset:38912
	ds_read_b128 v[240:243], v134 offset:39936
	buffer_load_dwordx4 v141, s[12:15], s53 offen lds
	s_mov_b32 m0, s42
	s_nop 0
	buffer_load_dwordx4 v143, s[12:15], s53 offen lds
	s_waitcnt vmcnt(18)
	s_waitcnt lgkmcnt(0)
	s_barrier
	s_setprio 1
	s_waitcnt lgkmcnt(7)
	v_mfma_f32_16x16x32_bf16 v[58:61], v[10:13], v[18:21], v[66:69]
	s_waitcnt lgkmcnt(6)
	v_mfma_f32_16x16x32_bf16 v[122:125], v[22:25], v[26:29], v[58:61]
	v_mfma_f32_16x16x32_bf16 v[58:61], v[30:33], v[18:21], v[70:73]
	v_mfma_f32_16x16x32_bf16 v[114:117], v[198:201], v[26:29], v[58:61]
	s_waitcnt lgkmcnt(5)
	v_mfma_f32_16x16x32_bf16 v[58:61], v[10:13], v[218:221], v[74:77]
	s_waitcnt lgkmcnt(4)
	v_mfma_f32_16x16x32_bf16 v[106:109], v[22:25], v[222:225], v[58:61]
	v_mfma_f32_16x16x32_bf16 v[58:61], v[30:33], v[218:221], v[78:81]
	v_mfma_f32_16x16x32_bf16 v[98:101], v[198:201], v[222:225], v[58:61]
	s_waitcnt lgkmcnt(3)
	v_mfma_f32_16x16x32_bf16 v[58:61], v[10:13], v[226:229], v[82:85]
	s_waitcnt lgkmcnt(2)
	v_mfma_f32_16x16x32_bf16 v[90:93], v[22:25], v[232:235], v[58:61]
	v_mfma_f32_16x16x32_bf16 v[58:61], v[30:33], v[226:229], v[86:89]
	v_mfma_f32_16x16x32_bf16 v[82:85], v[198:201], v[232:235], v[58:61]
	s_waitcnt lgkmcnt(1)
	v_mfma_f32_16x16x32_bf16 v[58:61], v[10:13], v[236:239], v[94:97]
	s_waitcnt lgkmcnt(0)
	v_mfma_f32_16x16x32_bf16 v[74:77], v[22:25], v[240:243], v[58:61]
	v_mfma_f32_16x16x32_bf16 v[58:61], v[30:33], v[236:239], v[102:105]
	v_mfma_f32_16x16x32_bf16 v[58:61], v[198:201], v[240:243], v[58:61]
	s_setprio 0
	s_setprio 1
	v_mfma_f32_16x16x32_bf16 v[66:69], v[202:205], v[18:21], v[110:113]
	v_mfma_f32_16x16x32_bf16 v[18:21], v[210:213], v[18:21], v[34:37]
	v_mfma_f32_16x16x32_bf16 v[118:121], v[214:217], v[26:29], v[18:21]
	v_mfma_f32_16x16x32_bf16 v[18:21], v[202:205], v[218:221], v[38:41]
	v_mfma_f32_16x16x32_bf16 v[110:113], v[206:209], v[222:225], v[18:21]
	v_mfma_f32_16x16x32_bf16 v[18:21], v[210:213], v[218:221], v[42:45]
	v_mfma_f32_16x16x32_bf16 v[102:105], v[214:217], v[222:225], v[18:21]
	v_mfma_f32_16x16x32_bf16 v[18:21], v[202:205], v[226:229], v[46:49]
	v_mfma_f32_16x16x32_bf16 v[94:97], v[206:209], v[232:235], v[18:21]
	v_mfma_f32_16x16x32_bf16 v[18:21], v[210:213], v[226:229], v[50:53]
	v_mfma_f32_16x16x32_bf16 v[86:89], v[214:217], v[232:235], v[18:21]
	v_mfma_f32_16x16x32_bf16 v[18:21], v[202:205], v[236:239], v[54:57]
	v_mfma_f32_16x16x32_bf16 v[78:81], v[206:209], v[240:243], v[18:21]
	v_mfma_f32_16x16x32_bf16 v[18:21], v[210:213], v[236:239], v[62:65]
	v_mfma_f32_16x16x32_bf16 v[126:129], v[206:209], v[26:29], v[66:69]
	v_mfma_f32_16x16x32_bf16 v[70:73], v[214:217], v[240:243], v[18:21]
	s_setprio 0
	s_barrier
	s_mov_b32 m0, s44
	s_add_i32 s17, s60, 0x180
	ds_read_b128 v[38:41], v134 offset:49152
	ds_read_b128 v[46:49], v134 offset:50176
	ds_read_b128 v[218:221], v134 offset:51200
	ds_read_b128 v[222:225], v134 offset:52224
	ds_read_b128 v[226:229], v134 offset:53248
	ds_read_b128 v[232:235], v134 offset:54272
	ds_read_b128 v[236:239], v134 offset:55296
	ds_read_b128 v[240:243], v134 offset:56320
	buffer_load_dwordx4 v130, s[12:15], s17 offen lds
	s_mov_b32 m0, s45
	s_nop 0
	buffer_load_dwordx4 v131, s[12:15], s17 offen lds
	s_add_i32 s17, s60, 0x40180
	s_mov_b32 m0, s49
	s_nop 0
	buffer_load_dwordx4 v130, s[12:15], s17 offen lds
	s_mov_b32 m0, s50
	s_nop 0
	buffer_load_dwordx4 v131, s[12:15], s17 offen lds
	s_mov_b32 s17, 0x8800180
	s_mov_b32 m0, s46
	s_nop 0
	buffer_load_dwordx4 v142, s[12:15], s17 offen lds
	s_mov_b32 m0, s48
	s_nop 0
	buffer_load_dwordx4 v144, s[12:15], s17 offen lds
	s_waitcnt vmcnt(14)
	s_waitcnt lgkmcnt(0)
	s_barrier
	s_setprio 1
	s_waitcnt lgkmcnt(7)
	v_mfma_f32_16x16x32_bf16 v[18:21], v[10:13], v[38:41], v[146:149]
	s_waitcnt lgkmcnt(6)
	v_mfma_f32_16x16x32_bf16 v[62:65], v[22:25], v[46:49], v[18:21]
	v_mfma_f32_16x16x32_bf16 v[18:21], v[30:33], v[38:41], v[150:153]
	v_mfma_f32_16x16x32_bf16 v[50:53], v[198:201], v[46:49], v[18:21]
	s_waitcnt lgkmcnt(5)
	v_mfma_f32_16x16x32_bf16 v[18:21], v[10:13], v[218:221], v[154:157]
	s_waitcnt lgkmcnt(4)
	v_mfma_f32_16x16x32_bf16 v[42:45], v[22:25], v[222:225], v[18:21]
	v_mfma_f32_16x16x32_bf16 v[18:21], v[30:33], v[218:221], v[158:161]
	v_mfma_f32_16x16x32_bf16 v[34:37], v[198:201], v[222:225], v[18:21]
	s_waitcnt lgkmcnt(3)
	v_mfma_f32_16x16x32_bf16 v[18:21], v[10:13], v[226:229], v[162:165]
	s_waitcnt lgkmcnt(1)
	v_mfma_f32_16x16x32_bf16 v[2:5], v[10:13], v[236:239], v[2:5]
	v_mfma_f32_16x16x32_bf16 v[26:29], v[22:25], v[232:235], v[18:21]
	v_mfma_f32_16x16x32_bf16 v[18:21], v[30:33], v[226:229], v[166:169]
	s_waitcnt lgkmcnt(0)
	v_mfma_f32_16x16x32_bf16 v[10:13], v[22:25], v[240:243], v[2:5]
	v_mfma_f32_16x16x32_bf16 v[2:5], v[30:33], v[236:239], v[6:9]
	v_mfma_f32_16x16x32_bf16 v[18:21], v[198:201], v[232:235], v[18:21]
	v_mfma_f32_16x16x32_bf16 v[2:5], v[198:201], v[240:243], v[2:5]
	s_setprio 0
	s_setprio 1
	v_mfma_f32_16x16x32_bf16 v[6:9], v[202:205], v[38:41], v[14:17]
	v_mfma_f32_16x16x32_bf16 v[66:69], v[206:209], v[46:49], v[6:9]
	v_mfma_f32_16x16x32_bf16 v[6:9], v[210:213], v[38:41], v[170:173]
	v_mfma_f32_16x16x32_bf16 v[54:57], v[214:217], v[46:49], v[6:9]
	v_mfma_f32_16x16x32_bf16 v[6:9], v[202:205], v[218:221], v[174:177]
	v_mfma_f32_16x16x32_bf16 v[46:49], v[206:209], v[222:225], v[6:9]
	v_mfma_f32_16x16x32_bf16 v[6:9], v[210:213], v[218:221], v[178:181]
	v_mfma_f32_16x16x32_bf16 v[38:41], v[214:217], v[222:225], v[6:9]
	v_mfma_f32_16x16x32_bf16 v[6:9], v[202:205], v[226:229], v[182:185]
	v_mfma_f32_16x16x32_bf16 v[30:33], v[206:209], v[232:235], v[6:9]
	v_mfma_f32_16x16x32_bf16 v[6:9], v[210:213], v[226:229], v[186:189]
	v_mfma_f32_16x16x32_bf16 v[22:25], v[214:217], v[232:235], v[6:9]
	v_mfma_f32_16x16x32_bf16 v[6:9], v[202:205], v[236:239], v[190:193]
	v_mfma_f32_16x16x32_bf16 v[14:17], v[206:209], v[240:243], v[6:9]
	v_mfma_f32_16x16x32_bf16 v[6:9], v[210:213], v[236:239], v[194:197]
	v_mfma_f32_16x16x32_bf16 v[6:9], v[214:217], v[240:243], v[6:9]
	s_setprio 0
	s_barrier
	s_mov_b32 s61, 0
	.p2alignl 6, 3212836864

;     __device__ __forceinline__ bool next(int i, pg8::Unit& u) const {
;         const int L = i * G + vcu; if (L >= NBt * NPN) return false;
;         const int blk = L / NPN, pn = L - blk * NPN; u.pm = blk; u.pn = pn;
;         if (blk < NBr) { const int w = tb[blk]; u.aux = GATHER ? i : w; u.B = Bexp + (unsigned)(w >> 16) * bstride + (unsigned)pn * 256u * ldb * 2u; }
;         else { u.aux = GATHER ? i : -1; u.B = Bsh + (unsigned)pn * 256u * ldb * 2u; }
;         u.A = GATHER ? Asrc : Asrc + (unsigned)blk * 256u * lda * 2u; return true;
.LBB0_876:
	s_lshl_b32 s16, s56, 2
	s_lshl_b32 s17, s56, 17
	s_sub_i32 s16, s52, s16
	s_add_i32 s17, s17, 0xcc00000
	.p2alignl 6, 3212836864

.LBB0_1029:
	ds_read_b128 v[2:5], v205
	ds_read_b128 v[6:9], v205 offset:1024
	ds_read_b128 v[10:13], v205 offset:2048
	ds_read_b128 v[14:17], v205 offset:3072
	ds_read_b128 v[18:21], v206
	ds_read_b128 v[22:25], v206 offset:1024
	ds_read_b128 v[26:29], v206 offset:2048
	ds_read_b128 v[30:33], v206 offset:3072
	s_add_i32 s1, s5, 0x100
	s_add_i32 s0, s5, 0x180
	s_add_i32 s30, s48, 0x100
	s_add_i32 s31, s5, 0x80
	s_mov_b32 s12, s38
	s_mov_b32 m0, s77
	ds_read_b128 v[34:37], v207
	ds_read_b128 v[38:41], v207 offset:1024
	ds_read_b128 v[42:45], v207 offset:2048
	ds_read_b128 v[46:49], v207 offset:3072
	ds_read_b128 v[50:53], v207 offset:4096
	ds_read_b128 v[54:57], v207 offset:5120
	ds_read_b128 v[58:61], v207 offset:6144
	ds_read_b128 v[62:65], v207 offset:7168
	buffer_load_dwordx4 v202, s[12:15], s31 offen lds
	s_mov_b32 m0, s78
	s_nop 0
	buffer_load_dwordx4 v204, s[12:15], s31 offen lds
	s_waitcnt vmcnt(26)
	s_waitcnt lgkmcnt(0)
	s_barrier
	s_setprio 1
	s_waitcnt lgkmcnt(0)
	v_mfma_f32_16x16x32_bf16 v[66:69], v[2:5], v[34:37], 0
	v_mfma_f32_16x16x32_bf16 v[70:73], v[10:13], v[34:37], 0
	v_mfma_f32_16x16x32_bf16 v[74:77], v[2:5], v[42:45], 0
	v_mfma_f32_16x16x32_bf16 v[78:81], v[10:13], v[42:45], 0
	v_mfma_f32_16x16x32_bf16 v[82:85], v[2:5], v[50:53], 0
	v_mfma_f32_16x16x32_bf16 v[86:89], v[10:13], v[50:53], 0
	v_mfma_f32_16x16x32_bf16 v[134:137], v[6:9], v[38:41], v[66:69]
	v_mfma_f32_16x16x32_bf16 v[146:149], v[14:17], v[38:41], v[70:73]
	v_mfma_f32_16x16x32_bf16 v[150:153], v[6:9], v[46:49], v[74:77]
	v_mfma_f32_16x16x32_bf16 v[78:81], v[14:17], v[46:49], v[78:81]
	v_mfma_f32_16x16x32_bf16 v[82:85], v[6:9], v[54:57], v[82:85]
	v_mfma_f32_16x16x32_bf16 v[86:89], v[14:17], v[54:57], v[86:89]
	v_mfma_f32_16x16x32_bf16 v[90:93], v[2:5], v[58:61], 0
	v_mfma_f32_16x16x32_bf16 v[94:97], v[10:13], v[58:61], 0
	v_mfma_f32_16x16x32_bf16 v[90:93], v[6:9], v[62:65], v[90:93]
	v_mfma_f32_16x16x32_bf16 v[94:97], v[14:17], v[62:65], v[94:97]
	s_setprio 0
	s_setprio 1
	v_mfma_f32_16x16x32_bf16 v[98:101], v[18:21], v[34:37], 0
	v_mfma_f32_16x16x32_bf16 v[34:37], v[26:29], v[34:37], 0
	v_mfma_f32_16x16x32_bf16 v[102:105], v[30:33], v[38:41], v[34:37]
	v_mfma_f32_16x16x32_bf16 v[34:37], v[18:21], v[42:45], 0
	v_mfma_f32_16x16x32_bf16 v[106:109], v[22:25], v[46:49], v[34:37]
	v_mfma_f32_16x16x32_bf16 v[34:37], v[26:29], v[42:45], 0
	v_mfma_f32_16x16x32_bf16 v[110:113], v[30:33], v[46:49], v[34:37]
	v_mfma_f32_16x16x32_bf16 v[34:37], v[18:21], v[50:53], 0
	v_mfma_f32_16x16x32_bf16 v[114:117], v[22:25], v[54:57], v[34:37]
	v_mfma_f32_16x16x32_bf16 v[34:37], v[26:29], v[50:53], 0
	v_mfma_f32_16x16x32_bf16 v[118:121], v[30:33], v[54:57], v[34:37]
	v_mfma_f32_16x16x32_bf16 v[34:37], v[18:21], v[58:61], 0
	v_mfma_f32_16x16x32_bf16 v[98:101], v[22:25], v[38:41], v[98:101]
	v_mfma_f32_16x16x32_bf16 v[122:125], v[22:25], v[62:65], v[34:37]
	v_mfma_f32_16x16x32_bf16 v[34:37], v[26:29], v[58:61], 0
	v_mfma_f32_16x16x32_bf16 v[126:129], v[30:33], v[62:65], v[34:37]
	s_setprio 0
	s_barrier
	s_mov_b32 m0, s58
	s_nop 3
	ds_read_b128 v[34:37], v207 offset:16384
	ds_read_b128 v[38:41], v207 offset:17408
	ds_read_b128 v[42:45], v207 offset:18432
	ds_read_b128 v[46:49], v207 offset:19456
	ds_read_b128 v[50:53], v207 offset:20480
	ds_read_b128 v[54:57], v207 offset:21504
	ds_read_b128 v[58:61], v207 offset:22528
	ds_read_b128 v[62:65], v207 offset:23552
	buffer_load_dwordx4 v1, s[12:15], s30 offen lds
	s_mov_b32 m0, s59
	s_nop 0
	buffer_load_dwordx4 v200, s[12:15], s30 offen lds
	s_add_i32 s30, s48, 0x10100
	s_mov_b32 m0, s60
	s_nop 0
	buffer_load_dwordx4 v1, s[12:15], s30 offen lds
	s_mov_b32 m0, s61
	s_nop 0
	buffer_load_dwordx4 v200, s[12:15], s30 offen lds
	s_mov_b32 m0, s57
	s_nop 0
	buffer_load_dwordx4 v201, s[12:15], s1 offen lds
	s_mov_b32 m0, s62
	s_nop 0
	buffer_load_dwordx4 v203, s[12:15], s1 offen lds
	s_waitcnt vmcnt(30)
	s_waitcnt lgkmcnt(0)
	s_barrier
	s_setprio 1
	s_waitcnt lgkmcnt(0)
	v_mfma_f32_16x16x32_bf16 v[130:133], v[2:5], v[34:37], 0
	v_mfma_f32_16x16x32_bf16 v[138:141], v[6:9], v[38:41], v[130:133]
	v_mfma_f32_16x16x32_bf16 v[130:133], v[10:13], v[34:37], 0
	v_mfma_f32_16x16x32_bf16 v[142:145], v[14:17], v[38:41], v[130:133]
	v_mfma_f32_16x16x32_bf16 v[130:133], v[2:5], v[42:45], 0
	v_mfma_f32_16x16x32_bf16 v[154:157], v[6:9], v[46:49], v[130:133]
	v_mfma_f32_16x16x32_bf16 v[130:133], v[10:13], v[42:45], 0
	v_mfma_f32_16x16x32_bf16 v[158:161], v[14:17], v[46:49], v[130:133]
	v_mfma_f32_16x16x32_bf16 v[130:133], v[2:5], v[50:53], 0
	v_mfma_f32_16x16x32_bf16 v[2:5], v[2:5], v[58:61], 0
	v_mfma_f32_16x16x32_bf16 v[170:173], v[6:9], v[54:57], v[130:133]
	v_mfma_f32_16x16x32_bf16 v[2:5], v[6:9], v[62:65], v[2:5]
	v_mfma_f32_16x16x32_bf16 v[6:9], v[10:13], v[58:61], 0
	v_mfma_f32_16x16x32_bf16 v[130:133], v[10:13], v[50:53], 0
	v_mfma_f32_16x16x32_bf16 v[6:9], v[14:17], v[62:65], v[6:9]
	v_mfma_f32_16x16x32_bf16 v[174:177], v[14:17], v[54:57], v[130:133]
	s_setprio 0
	s_setprio 1
	v_mfma_f32_16x16x32_bf16 v[10:13], v[18:21], v[34:37], 0
	v_mfma_f32_16x16x32_bf16 v[178:181], v[22:25], v[38:41], v[10:13]
	v_mfma_f32_16x16x32_bf16 v[10:13], v[26:29], v[34:37], 0
	v_mfma_f32_16x16x32_bf16 v[182:185], v[30:33], v[38:41], v[10:13]
	v_mfma_f32_16x16x32_bf16 v[10:13], v[18:21], v[42:45], 0
	v_mfma_f32_16x16x32_bf16 v[186:189], v[22:25], v[46:49], v[10:13]
	v_mfma_f32_16x16x32_bf16 v[10:13], v[26:29], v[42:45], 0
	v_mfma_f32_16x16x32_bf16 v[190:193], v[30:33], v[46:49], v[10:13]
	v_mfma_f32_16x16x32_bf16 v[10:13], v[18:21], v[50:53], 0
	v_mfma_f32_16x16x32_bf16 v[212:215], v[22:25], v[54:57], v[10:13]
	v_mfma_f32_16x16x32_bf16 v[10:13], v[26:29], v[50:53], 0
	v_mfma_f32_16x16x32_bf16 v[216:219], v[30:33], v[54:57], v[10:13]
	v_mfma_f32_16x16x32_bf16 v[10:13], v[18:21], v[58:61], 0
	v_mfma_f32_16x16x32_bf16 v[220:223], v[22:25], v[62:65], v[10:13]
	v_mfma_f32_16x16x32_bf16 v[10:13], v[26:29], v[58:61], 0
	v_mfma_f32_16x16x32_bf16 v[224:227], v[30:33], v[62:65], v[10:13]
	s_setprio 0
	s_barrier
; template <class Epi, class Sched>
; __device__ __forceinline__ void gemm_phase(PG8_LAS unsigned char* lds, const void* wsbase, const int K, const int ldb, const Sched& S, const Epi& E) {
;     ...
;         PG8_ITER(0, PG8_FIRSTW + 2 + Epi::NVM, PG8_FIRSTW + 6 + Epi::NVM, PG8_FIRSTW + 2 + Epi::NVM, PG8_FIRSTW + 6);
;         for (int t = 2; t < nt; t += 2) PG8_ITER(t, 8 + PG8_SLK1, 8 + PG8_SLK2, 8 + PG8_SLK1, 8 + PG8_SLK2);
	ds_read_b128 v[232:235], v208
	ds_read_b128 v[236:239], v208 offset:1024
	ds_read_b128 v[240:243], v208 offset:2048
	ds_read_b128 v[244:247], v208 offset:3072
	ds_read_b128 v[248:251], v209
	ds_read_b128 v[228:231], v209 offset:1024
	ds_read_b128 v[194:197], v209 offset:2048
	ds_read_b128 v[66:69], v209 offset:3072
	s_mov_b32 m0, s63
	ds_read_b128 v[10:13], v207 offset:32768
	ds_read_b128 v[14:17], v207 offset:33792
	ds_read_b128 v[18:21], v207 offset:34816
	ds_read_b128 v[22:25], v207 offset:35840
	ds_read_b128 v[26:29], v207 offset:36864
	ds_read_b128 v[30:33], v207 offset:37888
	ds_read_b128 v[70:73], v207 offset:38912
	ds_read_b128 v[74:77], v207 offset:39936
	buffer_load_dwordx4 v202, s[12:15], s1 offen lds
	s_mov_b32 m0, s64
	s_nop 0
	buffer_load_dwordx4 v204, s[12:15], s1 offen lds
	s_waitcnt vmcnt(26)
	s_waitcnt lgkmcnt(0)
	s_barrier
	s_setprio 1
	s_waitcnt lgkmcnt(0)
	v_mfma_f32_16x16x32_bf16 v[34:37], v[232:235], v[10:13], v[134:137]
	v_mfma_f32_16x16x32_bf16 v[58:61], v[236:239], v[14:17], v[34:37]
	v_mfma_f32_16x16x32_bf16 v[34:37], v[240:243], v[10:13], v[146:149]
	v_mfma_f32_16x16x32_bf16 v[62:65], v[244:247], v[14:17], v[34:37]
	v_mfma_f32_16x16x32_bf16 v[34:37], v[232:235], v[18:21], v[150:153]
	v_mfma_f32_16x16x32_bf16 v[50:53], v[236:239], v[22:25], v[34:37]
	v_mfma_f32_16x16x32_bf16 v[34:37], v[240:243], v[18:21], v[78:81]
	v_mfma_f32_16x16x32_bf16 v[54:57], v[244:247], v[22:25], v[34:37]
	v_mfma_f32_16x16x32_bf16 v[34:37], v[232:235], v[26:29], v[82:85]
	v_mfma_f32_16x16x32_bf16 v[42:45], v[236:239], v[30:33], v[34:37]
	v_mfma_f32_16x16x32_bf16 v[34:37], v[240:243], v[26:29], v[86:89]
	v_mfma_f32_16x16x32_bf16 v[46:49], v[244:247], v[30:33], v[34:37]
	v_mfma_f32_16x16x32_bf16 v[34:37], v[232:235], v[70:73], v[90:93]
	v_mfma_f32_16x16x32_bf16 v[38:41], v[240:243], v[70:73], v[94:97]
	v_mfma_f32_16x16x32_bf16 v[34:37], v[236:239], v[74:77], v[34:37]
	v_mfma_f32_16x16x32_bf16 v[38:41], v[244:247], v[74:77], v[38:41]
	s_setprio 0
	s_setprio 1
	v_mfma_f32_16x16x32_bf16 v[78:81], v[248:251], v[10:13], v[98:101]
	v_mfma_f32_16x16x32_bf16 v[10:13], v[194:197], v[10:13], v[102:105]
	v_mfma_f32_16x16x32_bf16 v[162:165], v[66:69], v[14:17], v[10:13]
	v_mfma_f32_16x16x32_bf16 v[10:13], v[248:251], v[18:21], v[106:109]
	v_mfma_f32_16x16x32_bf16 v[150:153], v[228:231], v[22:25], v[10:13]
	v_mfma_f32_16x16x32_bf16 v[10:13], v[194:197], v[18:21], v[110:113]
	v_mfma_f32_16x16x32_bf16 v[146:149], v[66:69], v[22:25], v[10:13]
	v_mfma_f32_16x16x32_bf16 v[10:13], v[248:251], v[26:29], v[114:117]
	v_mfma_f32_16x16x32_bf16 v[134:137], v[228:231], v[30:33], v[10:13]
	v_mfma_f32_16x16x32_bf16 v[10:13], v[194:197], v[26:29], v[118:121]
	v_mfma_f32_16x16x32_bf16 v[130:133], v[66:69], v[30:33], v[10:13]
	v_mfma_f32_16x16x32_bf16 v[10:13], v[248:251], v[70:73], v[122:125]
	v_mfma_f32_16x16x32_bf16 v[118:121], v[228:231], v[74:77], v[10:13]
	v_mfma_f32_16x16x32_bf16 v[10:13], v[194:197], v[70:73], v[126:129]
	v_mfma_f32_16x16x32_bf16 v[166:169], v[228:231], v[14:17], v[78:81]
	v_mfma_f32_16x16x32_bf16 v[114:117], v[66:69], v[74:77], v[10:13]
	s_setprio 0
	s_barrier
	s_mov_b32 m0, s70
	s_add_i32 s1, s48, 0x180
	ds_read_b128 v[70:73], v207 offset:49152
	ds_read_b128 v[74:77], v207 offset:50176
	ds_read_b128 v[78:81], v207 offset:51200
	ds_read_b128 v[82:85], v207 offset:52224
	ds_read_b128 v[90:93], v207 offset:53248
	ds_read_b128 v[94:97], v207 offset:54272
	ds_read_b128 v[106:109], v207 offset:55296
	ds_read_b128 v[110:113], v207 offset:56320
	buffer_load_dwordx4 v1, s[12:15], s1 offen lds
	s_mov_b32 m0, s72
	s_nop 0
	buffer_load_dwordx4 v200, s[12:15], s1 offen lds
	s_add_i32 s1, s48, 0x10180
	s_mov_b32 m0, s75
	s_nop 0
	buffer_load_dwordx4 v1, s[12:15], s1 offen lds
	s_mov_b32 m0, s76
	s_nop 0
	buffer_load_dwordx4 v200, s[12:15], s1 offen lds
	s_mov_b32 m0, s73
	s_nop 0
	buffer_load_dwordx4 v201, s[12:15], s0 offen lds
	s_mov_b32 m0, s74
	s_nop 0
	buffer_load_dwordx4 v203, s[12:15], s0 offen lds
	s_waitcnt vmcnt(14)
	s_waitcnt lgkmcnt(0)
	s_barrier
	s_setprio 1
	s_waitcnt lgkmcnt(0)
	v_mfma_f32_16x16x32_bf16 v[10:13], v[232:235], v[70:73], v[138:141]
	v_mfma_f32_16x16x32_bf16 v[26:29], v[236:239], v[74:77], v[10:13]
	v_mfma_f32_16x16x32_bf16 v[10:13], v[240:243], v[70:73], v[142:145]
	v_mfma_f32_16x16x32_bf16 v[30:33], v[244:247], v[74:77], v[10:13]
	v_mfma_f32_16x16x32_bf16 v[10:13], v[232:235], v[78:81], v[154:157]
	v_mfma_f32_16x16x32_bf16 v[18:21], v[236:239], v[82:85], v[10:13]
	v_mfma_f32_16x16x32_bf16 v[10:13], v[240:243], v[78:81], v[158:161]
	v_mfma_f32_16x16x32_bf16 v[22:25], v[244:247], v[82:85], v[10:13]
	v_mfma_f32_16x16x32_bf16 v[10:13], v[232:235], v[90:93], v[170:173]
	v_mfma_f32_16x16x32_bf16 v[14:17], v[240:243], v[90:93], v[174:177]
	v_mfma_f32_16x16x32_bf16 v[2:5], v[232:235], v[106:109], v[2:5]
	v_mfma_f32_16x16x32_bf16 v[6:9], v[240:243], v[106:109], v[6:9]
	v_mfma_f32_16x16x32_bf16 v[10:13], v[236:239], v[94:97], v[10:13]
	v_mfma_f32_16x16x32_bf16 v[14:17], v[244:247], v[94:97], v[14:17]
	v_mfma_f32_16x16x32_bf16 v[2:5], v[236:239], v[110:113], v[2:5]
	v_mfma_f32_16x16x32_bf16 v[6:9], v[244:247], v[110:113], v[6:9]
	s_setprio 0
	s_setprio 1
	v_mfma_f32_16x16x32_bf16 v[86:89], v[248:251], v[70:73], v[178:181]
	v_mfma_f32_16x16x32_bf16 v[70:73], v[194:197], v[70:73], v[182:185]
	v_mfma_f32_16x16x32_bf16 v[98:101], v[66:69], v[74:77], v[70:73]
	v_mfma_f32_16x16x32_bf16 v[70:73], v[248:251], v[78:81], v[186:189]
	v_mfma_f32_16x16x32_bf16 v[102:105], v[228:231], v[74:77], v[86:89]
	v_mfma_f32_16x16x32_bf16 v[86:89], v[228:231], v[82:85], v[70:73]
	v_mfma_f32_16x16x32_bf16 v[70:73], v[194:197], v[78:81], v[190:193]
	v_mfma_f32_16x16x32_bf16 v[82:85], v[66:69], v[82:85], v[70:73]
	v_mfma_f32_16x16x32_bf16 v[70:73], v[248:251], v[90:93], v[212:215]
	v_mfma_f32_16x16x32_bf16 v[78:81], v[228:231], v[94:97], v[70:73]
	v_mfma_f32_16x16x32_bf16 v[70:73], v[194:197], v[90:93], v[216:219]
	v_mfma_f32_16x16x32_bf16 v[74:77], v[66:69], v[94:97], v[70:73]
	v_mfma_f32_16x16x32_bf16 v[70:73], v[248:251], v[106:109], v[220:223]
	v_mfma_f32_16x16x32_bf16 v[90:93], v[194:197], v[106:109], v[224:227]
	v_mfma_f32_16x16x32_bf16 v[70:73], v[228:231], v[110:113], v[70:73]
	v_mfma_f32_16x16x32_bf16 v[66:69], v[66:69], v[110:113], v[90:93]
	s_setprio 0
	s_barrier
	s_add_i32 s0, s48, 0x200
	s_add_i32 s1, s5, 0x200
	s_mov_b32 s5, 0
	.p2alignl 6, 3212836864

.LBB0_1112:
	s_waitcnt lgkmcnt(0)
	ds_read_b128 v[2:5], v135
	ds_read_b128 v[6:9], v135 offset:1024
	ds_read_b128 v[10:13], v135 offset:2048
	ds_read_b128 v[14:17], v135 offset:3072
	ds_read_b128 v[18:21], v136
	ds_read_b128 v[22:25], v136 offset:1024
	ds_read_b128 v[26:29], v136 offset:2048
	ds_read_b128 v[30:33], v136 offset:3072
	s_add_i32 s1, s2, 0x100
	s_add_i32 s0, s2, 0x180
	s_add_i32 s20, s3, 0x100
	s_add_i32 s21, s2, 0x80
	s_mov_b32 s12, s38
	s_mov_b32 m0, s57
	ds_read_b128 v[34:37], v137
	ds_read_b128 v[38:41], v137 offset:1024
	ds_read_b128 v[42:45], v137 offset:2048
	ds_read_b128 v[46:49], v137 offset:3072
	ds_read_b128 v[50:53], v137 offset:4096
	ds_read_b128 v[54:57], v137 offset:5120
	ds_read_b128 v[58:61], v137 offset:6144
	ds_read_b128 v[62:65], v137 offset:7168
	buffer_load_dwordx4 v132, s[12:15], s21 offen lds
	s_mov_b32 m0, s58
	s_nop 0
	buffer_load_dwordx4 v134, s[12:15], s21 offen lds
	s_waitcnt vmcnt(26)
	s_waitcnt lgkmcnt(0)
	s_barrier
	s_setprio 1
	s_waitcnt lgkmcnt(0)
	v_mfma_f32_16x16x32_bf16 v[66:69], v[2:5], v[34:37], 0
	v_mfma_f32_16x16x32_bf16 v[70:73], v[10:13], v[34:37], 0
	v_mfma_f32_16x16x32_bf16 v[74:77], v[2:5], v[42:45], 0
	v_mfma_f32_16x16x32_bf16 v[78:81], v[10:13], v[42:45], 0
	v_mfma_f32_16x16x32_bf16 v[82:85], v[2:5], v[50:53], 0
	v_mfma_f32_16x16x32_bf16 v[86:89], v[10:13], v[50:53], 0
	v_mfma_f32_16x16x32_bf16 v[90:93], v[2:5], v[58:61], 0
	v_mfma_f32_16x16x32_bf16 v[94:97], v[10:13], v[58:61], 0
	v_mfma_f32_16x16x32_bf16 v[66:69], v[6:9], v[38:41], v[66:69]
	v_mfma_f32_16x16x32_bf16 v[70:73], v[14:17], v[38:41], v[70:73]
	v_mfma_f32_16x16x32_bf16 v[74:77], v[6:9], v[46:49], v[74:77]
	v_mfma_f32_16x16x32_bf16 v[78:81], v[14:17], v[46:49], v[78:81]
	v_mfma_f32_16x16x32_bf16 v[82:85], v[6:9], v[54:57], v[82:85]
	v_mfma_f32_16x16x32_bf16 v[86:89], v[14:17], v[54:57], v[86:89]
	v_mfma_f32_16x16x32_bf16 v[90:93], v[6:9], v[62:65], v[90:93]
	v_mfma_f32_16x16x32_bf16 v[94:97], v[14:17], v[62:65], v[94:97]
	s_setprio 0
	s_setprio 1
	v_mfma_f32_16x16x32_bf16 v[98:101], v[18:21], v[34:37], 0
	v_mfma_f32_16x16x32_bf16 v[34:37], v[26:29], v[34:37], 0
	v_mfma_f32_16x16x32_bf16 v[106:109], v[22:25], v[38:41], v[98:101]
	v_mfma_f32_16x16x32_bf16 v[34:37], v[30:33], v[38:41], v[34:37]
	v_mfma_f32_16x16x32_bf16 v[38:41], v[18:21], v[42:45], 0
	v_mfma_f32_16x16x32_bf16 v[42:45], v[26:29], v[42:45], 0
	v_mfma_f32_16x16x32_bf16 v[38:41], v[22:25], v[46:49], v[38:41]
	v_mfma_f32_16x16x32_bf16 v[42:45], v[30:33], v[46:49], v[42:45]
	v_mfma_f32_16x16x32_bf16 v[46:49], v[18:21], v[50:53], 0
	v_mfma_f32_16x16x32_bf16 v[50:53], v[26:29], v[50:53], 0
	v_mfma_f32_16x16x32_bf16 v[46:49], v[22:25], v[54:57], v[46:49]
	v_mfma_f32_16x16x32_bf16 v[50:53], v[30:33], v[54:57], v[50:53]
	v_mfma_f32_16x16x32_bf16 v[54:57], v[18:21], v[58:61], 0
	v_mfma_f32_16x16x32_bf16 v[58:61], v[26:29], v[58:61], 0
	v_mfma_f32_16x16x32_bf16 v[54:57], v[22:25], v[62:65], v[54:57]
	v_mfma_f32_16x16x32_bf16 v[58:61], v[30:33], v[62:65], v[58:61]
	s_setprio 0
	s_barrier
	s_mov_b32 m0, s40
	ds_read_b128 v[62:65], v137 offset:16384
	ds_read_b128 v[98:101], v137 offset:17408
	ds_read_b128 v[102:105], v137 offset:18432
	ds_read_b128 v[110:113], v137 offset:19456
	ds_read_b128 v[114:117], v137 offset:20480
	ds_read_b128 v[118:121], v137 offset:21504
	ds_read_b128 v[122:125], v137 offset:22528
	ds_read_b128 v[126:129], v137 offset:23552
	buffer_load_dwordx4 v1, s[12:15], s20 offen lds
	s_mov_b32 m0, s41
	s_nop 0
	buffer_load_dwordx4 v130, s[12:15], s20 offen lds
	s_add_i32 s20, s3, 0x10100
	s_mov_b32 m0, s42
	s_nop 0
	buffer_load_dwordx4 v1, s[12:15], s20 offen lds
	s_mov_b32 m0, s43
	s_nop 0
	buffer_load_dwordx4 v130, s[12:15], s20 offen lds
	s_mov_b32 m0, s23
	s_nop 0
	buffer_load_dwordx4 v131, s[12:15], s1 offen lds
	s_mov_b32 m0, s44
	s_nop 0
	buffer_load_dwordx4 v133, s[12:15], s1 offen lds
	s_waitcnt vmcnt(30)
	s_waitcnt lgkmcnt(0)
	s_barrier
	s_setprio 1
	s_waitcnt lgkmcnt(0)
	v_mfma_f32_16x16x32_bf16 v[142:145], v[2:5], v[62:65], 0
	v_mfma_f32_16x16x32_bf16 v[150:153], v[2:5], v[102:105], 0
	v_mfma_f32_16x16x32_bf16 v[158:161], v[2:5], v[114:117], 0
	v_mfma_f32_16x16x32_bf16 v[2:5], v[2:5], v[122:125], 0
	v_mfma_f32_16x16x32_bf16 v[142:145], v[6:9], v[98:101], v[142:145]
	v_mfma_f32_16x16x32_bf16 v[150:153], v[6:9], v[110:113], v[150:153]
	v_mfma_f32_16x16x32_bf16 v[158:161], v[6:9], v[118:121], v[158:161]
	v_mfma_f32_16x16x32_bf16 v[2:5], v[6:9], v[126:129], v[2:5]
	v_mfma_f32_16x16x32_bf16 v[6:9], v[10:13], v[122:125], 0
	v_mfma_f32_16x16x32_bf16 v[146:149], v[10:13], v[62:65], 0
	v_mfma_f32_16x16x32_bf16 v[154:157], v[10:13], v[102:105], 0
	v_mfma_f32_16x16x32_bf16 v[162:165], v[10:13], v[114:117], 0
	v_mfma_f32_16x16x32_bf16 v[6:9], v[14:17], v[126:129], v[6:9]
	v_mfma_f32_16x16x32_bf16 v[146:149], v[14:17], v[98:101], v[146:149]
	v_mfma_f32_16x16x32_bf16 v[154:157], v[14:17], v[110:113], v[154:157]
	v_mfma_f32_16x16x32_bf16 v[162:165], v[14:17], v[118:121], v[162:165]
	s_setprio 0
	s_setprio 1
	v_mfma_f32_16x16x32_bf16 v[10:13], v[18:21], v[62:65], 0
	v_mfma_f32_16x16x32_bf16 v[14:17], v[26:29], v[62:65], 0
	v_mfma_f32_16x16x32_bf16 v[62:65], v[18:21], v[102:105], 0
	v_mfma_f32_16x16x32_bf16 v[166:169], v[22:25], v[110:113], v[62:65]
	v_mfma_f32_16x16x32_bf16 v[62:65], v[26:29], v[102:105], 0
	v_mfma_f32_16x16x32_bf16 v[170:173], v[30:33], v[110:113], v[62:65]
	v_mfma_f32_16x16x32_bf16 v[62:65], v[18:21], v[114:117], 0
	v_mfma_f32_16x16x32_bf16 v[18:21], v[18:21], v[122:125], 0
	v_mfma_f32_16x16x32_bf16 v[10:13], v[22:25], v[98:101], v[10:13]
	v_mfma_f32_16x16x32_bf16 v[14:17], v[30:33], v[98:101], v[14:17]
	v_mfma_f32_16x16x32_bf16 v[174:177], v[22:25], v[118:121], v[62:65]
	v_mfma_f32_16x16x32_bf16 v[62:65], v[26:29], v[114:117], 0
	v_mfma_f32_16x16x32_bf16 v[182:185], v[22:25], v[126:129], v[18:21]
	v_mfma_f32_16x16x32_bf16 v[18:21], v[26:29], v[122:125], 0
	v_mfma_f32_16x16x32_bf16 v[178:181], v[30:33], v[118:121], v[62:65]
	v_mfma_f32_16x16x32_bf16 v[186:189], v[30:33], v[126:129], v[18:21]
	s_setprio 0
	s_barrier
; template <class Epi, class Sched>
; __device__ __forceinline__ void gemm_phase(PG8_LAS unsigned char* lds, const void* wsbase, const int K, const int ldb, const Sched& S, const Epi& E) {
;     ...
;         PG8_ITER(0, PG8_FIRSTW + 2 + Epi::NVM, PG8_FIRSTW + 6 + Epi::NVM, PG8_FIRSTW + 2 + Epi::NVM, PG8_FIRSTW + 6);
;         for (int t = 2; t < nt; t += 2) PG8_ITER(t, 8 + PG8_SLK1, 8 + PG8_SLK2, 8 + PG8_SLK1, 8 + PG8_SLK2);
	ds_read_b128 v[26:29], v138
	ds_read_b128 v[30:33], v138 offset:1024
	ds_read_b128 v[62:65], v138 offset:2048
	ds_read_b128 v[190:193], v138 offset:3072
	ds_read_b128 v[194:197], v139
	ds_read_b128 v[198:201], v139 offset:1024
	ds_read_b128 v[202:205], v139 offset:2048
	ds_read_b128 v[206:209], v139 offset:3072
	s_mov_b32 m0, s45
	ds_read_b128 v[18:21], v137 offset:32768
	ds_read_b128 v[22:25], v137 offset:33792
	ds_read_b128 v[110:113], v137 offset:34816
	ds_read_b128 v[210:213], v137 offset:35840
	ds_read_b128 v[214:217], v137 offset:36864
	ds_read_b128 v[218:221], v137 offset:37888
	ds_read_b128 v[222:225], v137 offset:38912
	ds_read_b128 v[226:229], v137 offset:39936
	buffer_load_dwordx4 v132, s[12:15], s1 offen lds
	s_mov_b32 m0, s46
	s_nop 0
	buffer_load_dwordx4 v134, s[12:15], s1 offen lds
	s_waitcnt vmcnt(26)
	s_waitcnt lgkmcnt(0)
	s_barrier
	s_setprio 1
	s_waitcnt lgkmcnt(0)
	v_mfma_f32_16x16x32_bf16 v[66:69], v[26:29], v[18:21], v[66:69]
	v_mfma_f32_16x16x32_bf16 v[114:117], v[30:33], v[22:25], v[66:69]
	v_mfma_f32_16x16x32_bf16 v[66:69], v[62:65], v[18:21], v[70:73]
	v_mfma_f32_16x16x32_bf16 v[118:121], v[190:193], v[22:25], v[66:69]
	v_mfma_f32_16x16x32_bf16 v[66:69], v[26:29], v[110:113], v[74:77]
	v_mfma_f32_16x16x32_bf16 v[98:101], v[30:33], v[210:213], v[66:69]
	v_mfma_f32_16x16x32_bf16 v[66:69], v[62:65], v[110:113], v[78:81]
	v_mfma_f32_16x16x32_bf16 v[102:105], v[190:193], v[210:213], v[66:69]
	v_mfma_f32_16x16x32_bf16 v[66:69], v[26:29], v[214:217], v[82:85]
	v_mfma_f32_16x16x32_bf16 v[82:85], v[30:33], v[218:221], v[66:69]
	v_mfma_f32_16x16x32_bf16 v[66:69], v[62:65], v[214:217], v[86:89]
	v_mfma_f32_16x16x32_bf16 v[86:89], v[190:193], v[218:221], v[66:69]
	v_mfma_f32_16x16x32_bf16 v[66:69], v[26:29], v[222:225], v[90:93]
	v_mfma_f32_16x16x32_bf16 v[70:73], v[62:65], v[222:225], v[94:97]
	v_mfma_f32_16x16x32_bf16 v[66:69], v[30:33], v[226:229], v[66:69]
	v_mfma_f32_16x16x32_bf16 v[70:73], v[190:193], v[226:229], v[70:73]
	s_setprio 0
	s_setprio 1
	v_mfma_f32_16x16x32_bf16 v[74:77], v[194:197], v[18:21], v[106:109]
	v_mfma_f32_16x16x32_bf16 v[18:21], v[202:205], v[18:21], v[34:37]
	v_mfma_f32_16x16x32_bf16 v[126:129], v[206:209], v[22:25], v[18:21]
	v_mfma_f32_16x16x32_bf16 v[18:21], v[194:197], v[110:113], v[38:41]
	v_mfma_f32_16x16x32_bf16 v[106:109], v[198:201], v[210:213], v[18:21]
	v_mfma_f32_16x16x32_bf16 v[18:21], v[202:205], v[110:113], v[42:45]
	v_mfma_f32_16x16x32_bf16 v[110:113], v[206:209], v[210:213], v[18:21]
	v_mfma_f32_16x16x32_bf16 v[18:21], v[194:197], v[214:217], v[46:49]
	v_mfma_f32_16x16x32_bf16 v[90:93], v[198:201], v[218:221], v[18:21]
	v_mfma_f32_16x16x32_bf16 v[18:21], v[202:205], v[214:217], v[50:53]
	v_mfma_f32_16x16x32_bf16 v[94:97], v[206:209], v[218:221], v[18:21]
	v_mfma_f32_16x16x32_bf16 v[18:21], v[194:197], v[222:225], v[54:57]
	v_mfma_f32_16x16x32_bf16 v[122:125], v[198:201], v[22:25], v[74:77]
	v_mfma_f32_16x16x32_bf16 v[74:77], v[198:201], v[226:229], v[18:21]
	v_mfma_f32_16x16x32_bf16 v[18:21], v[202:205], v[222:225], v[58:61]
	v_mfma_f32_16x16x32_bf16 v[78:81], v[206:209], v[226:229], v[18:21]
	s_setprio 0
	s_barrier
	s_mov_b32 m0, s50
	s_add_i32 s1, s3, 0x180
	ds_read_b128 v[42:45], v137 offset:49152
	ds_read_b128 v[46:49], v137 offset:50176
	ds_read_b128 v[210:213], v137 offset:51200
	ds_read_b128 v[214:217], v137 offset:52224
	ds_read_b128 v[218:221], v137 offset:53248
	ds_read_b128 v[222:225], v137 offset:54272
	ds_read_b128 v[226:229], v137 offset:55296
	ds_read_b128 v[230:233], v137 offset:56320
	buffer_load_dwordx4 v1, s[12:15], s1 offen lds
	s_mov_b32 m0, s51
	s_nop 0
	buffer_load_dwordx4 v130, s[12:15], s1 offen lds
	s_add_i32 s1, s3, 0x10180
	s_mov_b32 m0, s55
	s_nop 0
	buffer_load_dwordx4 v1, s[12:15], s1 offen lds
	s_mov_b32 m0, s56
	s_nop 0
	buffer_load_dwordx4 v130, s[12:15], s1 offen lds
	s_mov_b32 m0, s52
	s_nop 0
	buffer_load_dwordx4 v131, s[12:15], s0 offen lds
	s_mov_b32 m0, s53
	s_nop 0
	buffer_load_dwordx4 v133, s[12:15], s0 offen lds
	s_waitcnt vmcnt(14)
	s_waitcnt lgkmcnt(0)
	s_barrier
	s_setprio 1
	s_waitcnt lgkmcnt(0)
	v_mfma_f32_16x16x32_bf16 v[18:21], v[26:29], v[42:45], v[142:145]
	v_mfma_f32_16x16x32_bf16 v[50:53], v[30:33], v[46:49], v[18:21]
	v_mfma_f32_16x16x32_bf16 v[18:21], v[62:65], v[42:45], v[146:149]
	v_mfma_f32_16x16x32_bf16 v[54:57], v[190:193], v[46:49], v[18:21]
	v_mfma_f32_16x16x32_bf16 v[18:21], v[26:29], v[210:213], v[150:153]
	v_mfma_f32_16x16x32_bf16 v[34:37], v[30:33], v[214:217], v[18:21]
	v_mfma_f32_16x16x32_bf16 v[18:21], v[62:65], v[210:213], v[154:157]
	v_mfma_f32_16x16x32_bf16 v[38:41], v[190:193], v[214:217], v[18:21]
	v_mfma_f32_16x16x32_bf16 v[18:21], v[26:29], v[218:221], v[158:161]
	v_mfma_f32_16x16x32_bf16 v[22:25], v[62:65], v[218:221], v[162:165]
	v_mfma_f32_16x16x32_bf16 v[2:5], v[26:29], v[226:229], v[2:5]
	v_mfma_f32_16x16x32_bf16 v[6:9], v[62:65], v[226:229], v[6:9]
	v_mfma_f32_16x16x32_bf16 v[18:21], v[30:33], v[222:225], v[18:21]
	v_mfma_f32_16x16x32_bf16 v[22:25], v[190:193], v[222:225], v[22:25]
	v_mfma_f32_16x16x32_bf16 v[2:5], v[30:33], v[230:233], v[2:5]
	v_mfma_f32_16x16x32_bf16 v[6:9], v[190:193], v[230:233], v[6:9]
	s_setprio 0
	s_setprio 1
	v_mfma_f32_16x16x32_bf16 v[10:13], v[194:197], v[42:45], v[10:13]
	v_mfma_f32_16x16x32_bf16 v[58:61], v[198:201], v[46:49], v[10:13]
	v_mfma_f32_16x16x32_bf16 v[10:13], v[202:205], v[42:45], v[14:17]
	v_mfma_f32_16x16x32_bf16 v[62:65], v[206:209], v[46:49], v[10:13]
	v_mfma_f32_16x16x32_bf16 v[10:13], v[194:197], v[210:213], v[166:169]
	v_mfma_f32_16x16x32_bf16 v[42:45], v[198:201], v[214:217], v[10:13]
	v_mfma_f32_16x16x32_bf16 v[10:13], v[202:205], v[210:213], v[170:173]
	v_mfma_f32_16x16x32_bf16 v[46:49], v[206:209], v[214:217], v[10:13]
	v_mfma_f32_16x16x32_bf16 v[10:13], v[194:197], v[218:221], v[174:177]
	v_mfma_f32_16x16x32_bf16 v[26:29], v[198:201], v[222:225], v[10:13]
	v_mfma_f32_16x16x32_bf16 v[10:13], v[202:205], v[218:221], v[178:181]
	v_mfma_f32_16x16x32_bf16 v[30:33], v[206:209], v[222:225], v[10:13]
	v_mfma_f32_16x16x32_bf16 v[10:13], v[194:197], v[226:229], v[182:185]
	v_mfma_f32_16x16x32_bf16 v[14:17], v[202:205], v[226:229], v[186:189]
	v_mfma_f32_16x16x32_bf16 v[10:13], v[198:201], v[230:233], v[10:13]
	v_mfma_f32_16x16x32_bf16 v[14:17], v[206:209], v[230:233], v[14:17]
	s_setprio 0
	s_barrier
	s_add_i32 s0, s3, 0x200
	s_add_i32 s1, s2, 0x200
	s_mov_b32 s2, 0
	.p2alignl 6, 3212836864

; #define WAIT_BAR(N) asm volatile("s_waitcnt vmcnt(" #N ") lgkmcnt(0)\n\ts_barrier":::"memory")
;   #define DMA_K(t,slot) glds16s(Kh+(long)(t)*KVBLK*DM,kvo,(unsigned)__builtin_amdgcn_readfirstlane(kdst+(slot)))
;   #define DMA_V(t,slot) do{ glds16s(Vh+(long)(t)*KVBLK*DM,vvo,(unsigned)__builtin_amdgcn_readfirstlane(vdst+2*(slot))); glds16s(Vh+64+(long)(t)*KVBLK*DM,vvo,(unsigned)__builtin_amdgcn_readfirstlane(vdst+8192+2*(slot))); }while(0)
; template<int THRL> __device__ __forceinline__ void attn_unit(const bf16*Qu,const bf16*__restrict__ Kh,const bf16*__restrict__ Vh,bf16*Ou,const int NT,char*shm,const float kmax){
;   const int tid=threadIdx.x,lane=tid&63,r32=lane&31,hi=lane>>5; const int wid=__builtin_amdgcn_readfirstlane(tid>>6);
;   const bf16*Qw=Qu+(long)(wid*QBLK)*DM;
;   const unsigned lds0=(unsigned)(uintptr_t)shm;
;   float*wsf=(float*)(shm+LDS_WS)+wid*64;
;   const unsigned kvo=(unsigned)((lane*DM+wid*8)*2);
;   const unsigned vvo=(unsigned)(((16*(wid&3)+(lane>>2))*DM+(wid>>2)*32+(lane&3)*8)*2);
;   const unsigned kdst=lds0+LDS_K+wid*1024, vdst=lds0+LDS_V+wid*1024;
;     ...
;   const int vb0=(int)(lds0+LDS_V)+((lane>>4)&1)*32+(lane&3)*8+(4*hi+((lane&15)>>2))*64;
;   const char*Kbase=shm+LDS_K; bf16x8 kf[8];
;   const lds_cptr shm3=(lds_cptr)shm; const lds_cptr kp0=shm3+LDS_K+hi*1024+r32*16; const lds_cptr vp0=shm3+LDS_V+((lane>>4)&1)*32+(lane&3)*8+(4*hi+((lane&15)>>2))*64;
;   DMA_K(0,0);DMA_V(0,0);DMA_K(1,SLOTB);
;   bf16x8 qr[4];
;   #pragma unroll
;   for(int d0=0;d0<4;++d0)qr[d0]=*(const __attribute__((address_space(1))) bf16x8*)(&Qw[(long)r32*DM+d0*16+hi*8]);
;   float l_reg=0.f;f32x16 o[4];o[0]=f32x16{};o[1]=f32x16{};o[2]=f32x16{};o[3]=f32x16{};f32x16 negm;
;     ...
;   f32x16 pA0,pA1,pB0,pB1;
;   int sl_prev=0,sl_cur=0,sl_next=SLOTB;
;     ...
;   DMA_K(2,2*SLOTB);
;   WAIT_BAR(4);
;   { float q2=0.f;
;     #pragma unroll
;     for(int d0=0;d0<4;++d0){
;       #pragma unroll
;       for(int e=0;e<8;++e){ const float qv=__builtin_bit_cast(float,((unsigned)(unsigned short)qr[d0][e])<<16); q2=__builtin_fmaf(qv,qv,q2);} }
;     auto rq=__builtin_amdgcn_permlane32_swap(__float_as_uint(q2),__float_as_uint(q2),false,false); q2=__uint_as_float(rq[0])+__uint_as_float(rq[1]);
;     const float bound=__builtin_sqrtf(q2)*kmax*1.02f+1e-6f;
;     #pragma unroll
;     for(int r=0;r<16;++r)negm[r]=-bound; asm volatile("":"+v"(negm)); }
.LBB0_1242:
	s_ashr_i32 s0, s52, 3
	s_ashr_i32 s1, s0, 31
	s_lshl_b64 s[14:15], s[0:1], 12
	s_lshl_b32 s1, s53, 8
	s_and_b32 s56, s52, 7
	s_ashr_i32 s12, s1, 31
	s_add_u32 s14, s14, s1
	s_addc_u32 s15, s15, s12
	s_lshl_b64 s[16:17], s[14:15], 11
	s_add_u32 s1, s40, s16
	s_addc_u32 s12, s41, s17
	s_lshl_b32 s65, s56, 8
	s_add_u32 s1, s1, s65
	s_addc_u32 s12, s12, 0
	s_lshl_b32 s16, s54, 6
	s_ashr_i32 s17, s16, 31
	s_lshl_b64 s[20:21], s[16:17], 1
	s_add_u32 s30, s1, s20
	s_addc_u32 s31, s12, s21
	s_mul_i32 s69, s0, 0x880000
	s_mul_hi_i32 s68, s0, 0x880000
	s_add_u32 s0, s42, s69
	s_addc_u32 s1, s43, s68
	s_add_u32 s0, s0, s65
	s_addc_u32 s1, s1, 0
	s_add_u32 s18, s0, s20
	s_addc_u32 s19, s1, s21
	s_add_u32 s0, s44, s69
	s_addc_u32 s1, s45, s68
	s_add_u32 s16, s0, s65
	s_addc_u32 s17, s1, 0
	s_lshl_b32 s0, s52, 1
	s_add_i32 s0, s0, s54
	s_add_i32 s0, s0, 0x10000
	s_ashr_i32 s1, s0, 31
	s_lshl_b64 s[0:1], s[0:1], 2
	s_add_u32 s0, s36, s0
	v_readfirstlane_b32 s61, v0
	s_addc_u32 s1, s37, s1
	s_lshr_b32 s55, s61, 6
	s_lshl_b32 s12, s55, 5
	global_load_dword v2, v211, s[0:1]
	s_lshl_b64 s[0:1], s[12:13], 11
	s_add_u32 s0, s30, s0
	s_addc_u32 s1, s31, s1
	s_lshl_b32 s30, s55, 4
	v_add_u32_e32 v215, s30, v220
	v_and_or_b32 v3, s30, 48, v221
	s_lshr_b32 s30, s61, 3
	s_and_b32 s30, s30, 0x1fffffe0
	s_lshl_b32 s59, s55, 10
	s_cmp_lg_u32 0, -1
	v_lshl_add_u32 v3, v3, 10, s30
	s_cselect_b32 s30, 0, 0
	s_add_i32 s60, s59, s30
	s_add_i32 s57, s60, 0x6000
	v_or_b32_e32 v3, v3, v222
	s_mov_b32 s30, m0
	s_mov_b32 m0, s60
	s_nop 0
	global_load_lds_dwordx4 v215, s[18:19]
	s_mov_b32 m0, s30
	s_add_u32 s62, s16, 0x80
	v_lshlrev_b32_e32 v213, 1, v3
	s_mov_b32 s30, m0
	s_mov_b32 m0, s57
	s_nop 0
	global_load_lds_dwordx4 v213, s[16:17]
	s_mov_b32 m0, s30
	s_addc_u32 s63, s17, 0
	s_add_i32 s58, s60, 0x8000
	s_mov_b32 s30, m0
	s_mov_b32 m0, s58
	s_nop 0
	global_load_lds_dwordx4 v213, s[62:63]
	s_mov_b32 m0, s30
	s_add_u32 s62, s18, 0x20000
	s_addc_u32 s63, s19, 0
	s_add_i32 s30, s60, 0x2000
	s_mov_b32 s31, m0
	s_mov_b32 m0, s30
	s_nop 0
	global_load_lds_dwordx4 v215, s[62:63]
	s_mov_b32 m0, s31
	global_load_dwordx4 v[186:189], v233, s[0:1]
	global_load_dwordx4 v[178:181], v233, s[0:1] offset:32
	global_load_dwordx4 v[170:173], v233, s[0:1] offset:64
	global_load_dwordx4 v[162:165], v233, s[0:1] offset:96
	s_add_u32 s0, s18, 0x40000
	s_addc_u32 s1, s19, 0
	s_add_i32 s30, s60, 0x4000
	s_mov_b32 s31, m0
	s_mov_b32 m0, s30
	s_nop 0
	global_load_lds_dwordx4 v215, s[0:1]
	s_mov_b32 m0, s31
	s_waitcnt vmcnt(4) lgkmcnt(0)
	s_barrier
	v_mov_b32_e32 v217, 0
	s_mov_b32 s62, -1
	s_mov_b32 s66, 0
	s_movk_i32 s64, 0x2000
	s_movk_i32 s63, 0x4000
	v_mov_b32_e32 v38, v217
	v_mov_b32_e32 v39, v217
	v_mov_b32_e32 v40, v217
	v_mov_b32_e32 v41, v217
	v_mov_b32_e32 v42, v217
	v_mov_b32_e32 v43, v217
	v_mov_b32_e32 v44, v217
	v_mov_b32_e32 v45, v217
	v_mov_b32_e32 v46, v217
	v_mov_b32_e32 v47, v217
	v_mov_b32_e32 v48, v217
	v_mov_b32_e32 v49, v217
	v_mov_b32_e32 v50, 0
	v_mov_b32_e32 v51, v217
	v_mov_b32_e32 v52, v217
	v_mov_b32_e32 v53, v217
	v_mov_b32_e32 v54, v217
	v_mov_b32_e32 v55, v217
	v_mov_b32_e32 v56, v217
	v_mov_b32_e32 v57, v217
	v_mov_b32_e32 v58, v217
	v_mov_b32_e32 v59, v217
	v_mov_b32_e32 v60, v217
	v_mov_b32_e32 v61, v217
	v_mov_b32_e32 v62, v217
	v_mov_b32_e32 v63, v217
	v_mov_b32_e32 v64, v217
	v_mov_b32_e32 v65, v217
	s_waitcnt vmcnt(0)
	v_lshlrev_b32_e32 v3, 16, v186
	v_and_b32_e32 v4, 0xffff0000, v186
	v_fma_f32 v3, v3, v3, 0
	v_lshlrev_b32_e32 v5, 16, v187
	v_fmac_f32_e32 v3, v4, v4
	v_and_b32_e32 v6, 0xffff0000, v187
	v_fmac_f32_e32 v3, v5, v5
	v_lshlrev_b32_e32 v7, 16, v188
	v_fmac_f32_e32 v3, v6, v6
	v_and_b32_e32 v8, 0xffff0000, v188
	v_fmac_f32_e32 v3, v7, v7
	v_lshlrev_b32_e32 v9, 16, v189
	v_fmac_f32_e32 v3, v8, v8
	v_and_b32_e32 v10, 0xffff0000, v189
	v_fmac_f32_e32 v3, v9, v9
	v_lshlrev_b32_e32 v11, 16, v178
	v_fmac_f32_e32 v3, v10, v10
	v_and_b32_e32 v12, 0xffff0000, v178
	v_fmac_f32_e32 v3, v11, v11
	v_lshlrev_b32_e32 v13, 16, v179
	v_fmac_f32_e32 v3, v12, v12
	v_and_b32_e32 v14, 0xffff0000, v179
	v_fmac_f32_e32 v3, v13, v13
	v_lshlrev_b32_e32 v15, 16, v180
	v_fmac_f32_e32 v3, v14, v14
	v_and_b32_e32 v16, 0xffff0000, v180
	v_fmac_f32_e32 v3, v15, v15
	v_lshlrev_b32_e32 v17, 16, v181
	v_fmac_f32_e32 v3, v16, v16
	v_and_b32_e32 v18, 0xffff0000, v181
	v_fmac_f32_e32 v3, v17, v17
	v_lshlrev_b32_e32 v19, 16, v170
	v_fmac_f32_e32 v3, v18, v18
	v_and_b32_e32 v20, 0xffff0000, v170
	v_fmac_f32_e32 v3, v19, v19
	v_lshlrev_b32_e32 v21, 16, v171
	v_fmac_f32_e32 v3, v20, v20
	v_and_b32_e32 v22, 0xffff0000, v171
	v_fmac_f32_e32 v3, v21, v21
	v_lshlrev_b32_e32 v23, 16, v172
	v_fmac_f32_e32 v3, v22, v22
	v_and_b32_e32 v24, 0xffff0000, v172
	v_fmac_f32_e32 v3, v23, v23
	v_lshlrev_b32_e32 v25, 16, v173
	v_fmac_f32_e32 v3, v24, v24
	v_and_b32_e32 v26, 0xffff0000, v173
	v_fmac_f32_e32 v3, v25, v25
	v_lshlrev_b32_e32 v27, 16, v162
	v_fmac_f32_e32 v3, v26, v26
	v_and_b32_e32 v28, 0xffff0000, v162
	v_fmac_f32_e32 v3, v27, v27
	v_lshlrev_b32_e32 v29, 16, v163
	v_fmac_f32_e32 v3, v28, v28
	v_and_b32_e32 v30, 0xffff0000, v163
	v_fmac_f32_e32 v3, v29, v29
	v_lshlrev_b32_e32 v31, 16, v164
	v_fmac_f32_e32 v3, v30, v30
	v_and_b32_e32 v32, 0xffff0000, v164
	v_fmac_f32_e32 v3, v31, v31
	v_lshlrev_b32_e32 v33, 16, v165
	v_fmac_f32_e32 v3, v32, v32
	v_and_b32_e32 v34, 0xffff0000, v165
	v_fmac_f32_e32 v3, v33, v33
	v_fmac_f32_e32 v3, v34, v34
	v_mov_b32_e32 v4, v3
	s_nop 1
	v_permlane32_swap_b32_e32 v3, v4
	v_add_f32_e32 v3, v3, v4
	v_mul_f32_e32 v4, 0x4f800000, v3
	v_cmp_gt_f32_e32 vcc, s50, v3
	s_nop 1
	v_cndmask_b32_e32 v3, v3, v4, vcc
	v_sqrt_f32_e32 v4, v3
	s_nop 0
	v_add_u32_e32 v5, -1, v4
	v_add_u32_e32 v6, 1, v4
	v_fma_f32 v7, -v5, v4, v3
	v_fma_f32 v8, -v6, v4, v3
	v_cmp_ge_f32_e64 s[0:1], 0, v7
	s_nop 1
	v_cndmask_b32_e64 v4, v4, v5, s[0:1]
	v_cmp_lt_f32_e64 s[0:1], 0, v8
	s_nop 1
	v_cndmask_b32_e64 v4, v4, v6, s[0:1]
	v_mul_f32_e32 v5, 0x37800000, v4
	v_cndmask_b32_e32 v4, v4, v5, vcc
	v_cmp_class_f32_e32 vcc, v3, v234
	s_add_u32 s0, s18, 0x60000
	s_addc_u32 s1, s19, 0
	v_cndmask_b32_e32 v3, v4, v3, vcc
	v_mul_f32_e32 v2, v2, v3
	v_fmamk_f32 v2, v2, 0x3f828f5c, v235
	v_xor_b32_e32 v66, 0x80000000, v2
	v_mov_b32_e32 v67, v66
	v_mov_b32_e32 v68, v66
	v_mov_b32_e32 v69, v66
	v_mov_b32_e32 v70, v66
	v_mov_b32_e32 v71, v66
	v_mov_b32_e32 v72, v66
	v_mov_b32_e32 v73, v66
	v_mov_b32_e32 v74, v66
	v_mov_b32_e32 v75, v66
	v_mov_b32_e32 v76, v66
	v_mov_b32_e32 v77, v66
	v_mov_b32_e32 v78, v66
	v_mov_b32_e32 v79, v66
	v_mov_b32_e32 v80, v66
	v_mov_b32_e32 v81, v66
	ds_read_b128 v[2:5], v223
	ds_read_b128 v[34:37], v223 offset:512
	s_waitcnt lgkmcnt(1)
; #define WAIT_BAR(N) asm volatile("s_waitcnt vmcnt(" #N ") lgkmcnt(0)\n\ts_barrier":::"memory")
;   #define DMA_K(t,slot) glds16s(Kh+(long)(t)*KVBLK*DM,kvo,(unsigned)__builtin_amdgcn_readfirstlane(kdst+(slot)))
;   #define DMA_V(t,slot) do{ glds16s(Vh+(long)(t)*KVBLK*DM,vvo,(unsigned)__builtin_amdgcn_readfirstlane(vdst+2*(slot))); glds16s(Vh+64+(long)(t)*KVBLK*DM,vvo,(unsigned)__builtin_amdgcn_readfirstlane(vdst+8192+2*(slot))); }while(0)
;   #define CMASK(P0,P1,t) do{}while(0)
;   #define START(P0,P1) do{ _Pragma("unroll") for(int r=0;r<16;++r)P0[r]=__builtin_amdgcn_exp2f(P0[r]); }while(0)
;   #define ROT() do{sl_prev=sl_cur;sl_cur=sl_next;sl_next=(sl_next==(NSLOT-1)*SLOTB)?0:sl_next+SLOTB;}while(0)
; __device__ __forceinline__ void qkt(f32x16&p0,f32x16&p1,const char*Kslot,const bf16x8*qr,const f32x16&negm,int r32,int hi){
;   const char*kb=Kslot+hi*1024+r32*16;
;   #pragma unroll
;   for(int d0=0;d0<4;++d0){
;     const bf16x8 b0=*reinterpret_cast<const bf16x8*>(kb+d0*2048);
;     const bf16x8 b1=*reinterpret_cast<const bf16x8*>(kb+d0*2048+512);
;     if(d0==0){p0=__builtin_amdgcn_mfma_f32_32x32x16_bf16(b0,qr[0],negm,0,0,0);p1=__builtin_amdgcn_mfma_f32_32x32x16_bf16(b1,qr[0],negm,0,0,0);}
;     else{p0=__builtin_amdgcn_mfma_f32_32x32x16_bf16(b0,qr[d0],p0,0,0,0);p1=__builtin_amdgcn_mfma_f32_32x32x16_bf16(b1,qr[d0],p1,0,0,0);}}
; template<int THRL> __device__ __forceinline__ void attn_unit(const bf16*Qu,const bf16*__restrict__ Kh,const bf16*__restrict__ Vh,bf16*Ou,const int NT,char*shm,const float kmax){
;     ...
;   qkt(pA0,pA1,Kbase,qr,negm,r32,hi);asm volatile("s_nop 15\n\ts_nop 7":"+v"(pA0),"+v"(pA1));CMASK(pA0,pA1,0);
;   START(pA0,pA1);
;   _Pragma("unroll") for(int r=0;r<16;++r)pA1[r]=__builtin_amdgcn_exp2f(pA1[r]);
;   WAIT_BAR(0);
;   DMA_K(3,0);DMA_V(1,SLOTB);
;   ROT();
;   kload8(kf,kp0+sl_cur);
;   WAIT_BAR(3);
;   s16x4 vlo[8],vhi[8]; u32x4 pw0,pw1,pw2,pw3;
	v_mfma_f32_32x32x16_bf16 v[18:33], v[2:5], v[186:189], v[66:81]
	s_waitcnt lgkmcnt(0)
	v_mfma_f32_32x32x16_bf16 v[2:17], v[34:37], v[186:189], v[66:81]
	ds_read_b128 v[34:37], v223 offset:2048
	s_waitcnt lgkmcnt(0)
	v_mfma_f32_32x32x16_bf16 v[18:33], v[34:37], v[178:181], v[18:33]
	ds_read_b128 v[34:37], v223 offset:2560
	s_waitcnt lgkmcnt(0)
	v_mfma_f32_32x32x16_bf16 v[2:17], v[34:37], v[178:181], v[2:17]
	ds_read_b128 v[34:37], v223 offset:4096
	s_waitcnt lgkmcnt(0)
	v_mfma_f32_32x32x16_bf16 v[18:33], v[34:37], v[170:173], v[18:33]
	ds_read_b128 v[34:37], v223 offset:4608
	s_waitcnt lgkmcnt(0)
	v_mfma_f32_32x32x16_bf16 v[2:17], v[34:37], v[170:173], v[2:17]
	ds_read_b128 v[34:37], v223 offset:6144
	s_waitcnt lgkmcnt(0)
	v_mfma_f32_32x32x16_bf16 v[18:33], v[34:37], v[162:165], v[18:33]
	ds_read_b128 v[34:37], v223 offset:6656
	s_waitcnt lgkmcnt(0)
	v_mfma_f32_32x32x16_bf16 v[2:17], v[34:37], v[162:165], v[2:17]
	s_nop 15
	s_nop 7
	s_waitcnt vmcnt(0) lgkmcnt(0)
	s_barrier
	s_mov_b32 s30, m0
	s_mov_b32 m0, s60
	s_nop 0
	global_load_lds_dwordx4 v215, s[0:1]
	s_mov_b32 m0, s30
	s_add_u32 s0, s16, 0x20000
	s_addc_u32 s1, s17, 0
	s_add_i32 s30, s60, 0xa000
	s_mov_b32 s31, m0
	s_mov_b32 m0, s30
	s_nop 0
	global_load_lds_dwordx4 v213, s[0:1]
	s_mov_b32 m0, s31
	s_add_u32 s0, s16, 0x20080
	s_addc_u32 s1, s17, 0
	s_add_i32 s30, s60, 0xc000
	s_mov_b32 s31, m0
	s_mov_b32 m0, s30
	s_nop 0
	global_load_lds_dwordx4 v213, s[0:1]
	s_mov_b32 m0, s31
	ds_read_b128 v[114:117], v223 offset:8192
	ds_read_b128 v[202:205], v223 offset:8704
	ds_read_b128 v[198:201], v223 offset:10240
	ds_read_b128 v[194:197], v223 offset:10752
	ds_read_b128 v[158:161], v223 offset:12288
	ds_read_b128 v[154:157], v223 offset:12800
	ds_read_b128 v[150:153], v223 offset:14336
	ds_read_b128 v[146:149], v223 offset:14848
	v_exp_f32_e32 v98, v18
	v_exp_f32_e32 v99, v19
	v_exp_f32_e32 v100, v20
	v_exp_f32_e32 v101, v21
	v_exp_f32_e32 v102, v22
	v_exp_f32_e32 v103, v23
	v_exp_f32_e32 v104, v24
	v_exp_f32_e32 v105, v25
	v_exp_f32_e32 v106, v26
	v_exp_f32_e32 v107, v27
	v_exp_f32_e32 v108, v28
	v_exp_f32_e32 v109, v29
	v_exp_f32_e32 v110, v30
	v_exp_f32_e32 v111, v31
	v_exp_f32_e32 v112, v32
	v_exp_f32_e32 v113, v33
	v_exp_f32_e32 v82, v2
	v_exp_f32_e32 v83, v3
	v_exp_f32_e32 v84, v4
	v_exp_f32_e32 v85, v5
	v_exp_f32_e32 v86, v6
	v_exp_f32_e32 v87, v7
	v_exp_f32_e32 v88, v8
	v_exp_f32_e32 v89, v9
	v_exp_f32_e32 v90, v10
	v_exp_f32_e32 v91, v11
	v_exp_f32_e32 v92, v12
	v_exp_f32_e32 v93, v13
	v_exp_f32_e32 v94, v14
	v_exp_f32_e32 v95, v15
	v_exp_f32_e32 v96, v16
	v_exp_f32_e32 v97, v17
	s_waitcnt vmcnt(3) lgkmcnt(0)
	s_barrier
	s_or_b32 s0, s69, s65
	s_add_u32 s0, s48, s0
	s_addc_u32 s1, s49, s68
	v_mov_b32_e32 v34, 0
	v_mov_b32_e32 v35, v217
	v_mov_b32_e32 v36, v217
	v_mov_b32_e32 v37, v217
	v_mov_b32_e32 v2, 0
	v_mov_b32_e32 v3, v217
	v_mov_b32_e32 v4, v217
	v_mov_b32_e32 v5, v217
	v_mov_b32_e32 v6, v217
	v_mov_b32_e32 v7, v217
	v_mov_b32_e32 v8, v217
	v_mov_b32_e32 v9, v217
	v_mov_b32_e32 v10, v217
	v_mov_b32_e32 v11, v217
	v_mov_b32_e32 v12, v217
	v_mov_b32_e32 v13, v217
	v_mov_b32_e32 v14, v217
	v_mov_b32_e32 v15, v217
	v_mov_b32_e32 v16, v217
	v_mov_b32_e32 v17, v217
	v_mov_b32_e32 v18, 0
	v_mov_b32_e32 v19, v217
	v_mov_b32_e32 v20, v217
	v_mov_b32_e32 v21, v217
	v_mov_b32_e32 v22, v217
	v_mov_b32_e32 v23, v217
	v_mov_b32_e32 v24, v217
	v_mov_b32_e32 v25, v217
	v_mov_b32_e32 v26, v217
	v_mov_b32_e32 v27, v217
	v_mov_b32_e32 v28, v217
	v_mov_b32_e32 v29, v217
	v_mov_b32_e32 v30, v217
	v_mov_b32_e32 v31, v217
	v_mov_b32_e32 v32, v217
	v_mov_b32_e32 v33, v217
	.p2alignl 6, 3212836864

.LBB0_1382:
	ds_read_b128 v[2:5], v139
	ds_read_b128 v[6:9], v139 offset:1024
	ds_read_b128 v[10:13], v139 offset:2048
	ds_read_b128 v[14:17], v139 offset:3072
	ds_read_b128 v[18:21], v140
	ds_read_b128 v[22:25], v140 offset:1024
	ds_read_b128 v[26:29], v140 offset:2048
	ds_read_b128 v[30:33], v140 offset:3072
	s_add_i32 s17, s58, 0x100
	s_add_i32 s16, s58, 0x180
	s_add_i32 s30, s59, 0x100
	s_add_i32 s31, s58, 0x80
	s_mov_b32 m0, s50
	ds_read_b128 v[34:37], v141
	ds_read_b128 v[38:41], v141 offset:1024
	ds_read_b128 v[42:45], v141 offset:2048
	ds_read_b128 v[46:49], v141 offset:3072
	ds_read_b128 v[50:53], v141 offset:4096
	ds_read_b128 v[54:57], v141 offset:5120
	ds_read_b128 v[58:61], v141 offset:6144
	ds_read_b128 v[62:65], v141 offset:7168
	buffer_load_dwordx4 v136, s[12:15], s31 offen lds
	s_mov_b32 m0, s51
	s_nop 0
	buffer_load_dwordx4 v138, s[12:15], s31 offen lds
	s_waitcnt vmcnt(26)
	s_waitcnt lgkmcnt(0)
	s_barrier
	s_setprio 1
	s_waitcnt lgkmcnt(0)
	v_mfma_f32_16x16x32_bf16 v[90:93], v[2:5], v[58:61], 0
	v_mfma_f32_16x16x32_bf16 v[66:69], v[2:5], v[34:37], 0
	v_mfma_f32_16x16x32_bf16 v[70:73], v[10:13], v[34:37], 0
	v_mfma_f32_16x16x32_bf16 v[74:77], v[2:5], v[42:45], 0
	v_mfma_f32_16x16x32_bf16 v[78:81], v[10:13], v[42:45], 0
	v_mfma_f32_16x16x32_bf16 v[82:85], v[2:5], v[50:53], 0
	v_mfma_f32_16x16x32_bf16 v[86:89], v[10:13], v[50:53], 0
	v_mfma_f32_16x16x32_bf16 v[94:97], v[6:9], v[62:65], v[90:93]
	v_mfma_f32_16x16x32_bf16 v[90:93], v[10:13], v[58:61], 0
	v_mfma_f32_16x16x32_bf16 v[66:69], v[6:9], v[38:41], v[66:69]
	v_mfma_f32_16x16x32_bf16 v[70:73], v[14:17], v[38:41], v[70:73]
	v_mfma_f32_16x16x32_bf16 v[74:77], v[6:9], v[46:49], v[74:77]
	v_mfma_f32_16x16x32_bf16 v[78:81], v[14:17], v[46:49], v[78:81]
	v_mfma_f32_16x16x32_bf16 v[82:85], v[6:9], v[54:57], v[82:85]
	v_mfma_f32_16x16x32_bf16 v[86:89], v[14:17], v[54:57], v[86:89]
	v_mfma_f32_16x16x32_bf16 v[102:105], v[14:17], v[62:65], v[90:93]
	s_setprio 0
	s_setprio 1
	v_mfma_f32_16x16x32_bf16 v[90:93], v[18:21], v[34:37], 0
	v_mfma_f32_16x16x32_bf16 v[34:37], v[26:29], v[34:37], 0
	v_mfma_f32_16x16x32_bf16 v[110:113], v[22:25], v[38:41], v[90:93]
	v_mfma_f32_16x16x32_bf16 v[34:37], v[30:33], v[38:41], v[34:37]
	v_mfma_f32_16x16x32_bf16 v[38:41], v[18:21], v[42:45], 0
	v_mfma_f32_16x16x32_bf16 v[42:45], v[26:29], v[42:45], 0
	v_mfma_f32_16x16x32_bf16 v[38:41], v[22:25], v[46:49], v[38:41]
	v_mfma_f32_16x16x32_bf16 v[42:45], v[30:33], v[46:49], v[42:45]
	v_mfma_f32_16x16x32_bf16 v[46:49], v[18:21], v[50:53], 0
	v_mfma_f32_16x16x32_bf16 v[50:53], v[26:29], v[50:53], 0
	v_mfma_f32_16x16x32_bf16 v[46:49], v[22:25], v[54:57], v[46:49]
	v_mfma_f32_16x16x32_bf16 v[54:57], v[30:33], v[54:57], v[50:53]
	v_mfma_f32_16x16x32_bf16 v[50:53], v[18:21], v[58:61], 0
	v_mfma_f32_16x16x32_bf16 v[144:147], v[22:25], v[62:65], v[50:53]
	v_mfma_f32_16x16x32_bf16 v[50:53], v[26:29], v[58:61], 0
	v_mfma_f32_16x16x32_bf16 v[148:151], v[30:33], v[62:65], v[50:53]
	s_setprio 0
	s_barrier
	s_mov_b32 m0, s19
	s_nop 3
	ds_read_b128 v[50:53], v141 offset:16384
	ds_read_b128 v[58:61], v141 offset:17408
	ds_read_b128 v[62:65], v141 offset:18432
	ds_read_b128 v[90:93], v141 offset:19456
	ds_read_b128 v[98:101], v141 offset:20480
	ds_read_b128 v[106:109], v141 offset:21504
	ds_read_b128 v[114:117], v141 offset:22528
	ds_read_b128 v[118:121], v141 offset:23552
	buffer_load_dwordx4 v1, s[12:15], s30 offen lds
	s_mov_b32 m0, s20
	s_nop 0
	buffer_load_dwordx4 v134, s[12:15], s30 offen lds
	s_add_i32 s30, s59, 0x10100
	s_mov_b32 m0, s21
	s_nop 0
	buffer_load_dwordx4 v1, s[12:15], s30 offen lds
	s_mov_b32 m0, s22
	s_nop 0
	buffer_load_dwordx4 v134, s[12:15], s30 offen lds
	s_mov_b32 m0, s18
	s_nop 0
	buffer_load_dwordx4 v135, s[12:15], s17 offen lds
	s_mov_b32 m0, s23
	s_nop 0
	buffer_load_dwordx4 v137, s[12:15], s17 offen lds
	s_waitcnt vmcnt(30)
	s_waitcnt lgkmcnt(0)
	s_barrier
	s_setprio 1
	s_waitcnt lgkmcnt(0)
	v_mfma_f32_16x16x32_bf16 v[122:125], v[2:5], v[50:53], 0
	v_mfma_f32_16x16x32_bf16 v[152:155], v[6:9], v[58:61], v[122:125]
	v_mfma_f32_16x16x32_bf16 v[122:125], v[10:13], v[50:53], 0
	v_mfma_f32_16x16x32_bf16 v[156:159], v[14:17], v[58:61], v[122:125]
	v_mfma_f32_16x16x32_bf16 v[122:125], v[2:5], v[62:65], 0
	v_mfma_f32_16x16x32_bf16 v[160:163], v[6:9], v[90:93], v[122:125]
	v_mfma_f32_16x16x32_bf16 v[122:125], v[10:13], v[62:65], 0
	v_mfma_f32_16x16x32_bf16 v[164:167], v[14:17], v[90:93], v[122:125]
	v_mfma_f32_16x16x32_bf16 v[122:125], v[2:5], v[98:101], 0
	v_mfma_f32_16x16x32_bf16 v[2:5], v[2:5], v[114:117], 0
	v_mfma_f32_16x16x32_bf16 v[168:171], v[6:9], v[106:109], v[122:125]
	v_mfma_f32_16x16x32_bf16 v[2:5], v[6:9], v[118:121], v[2:5]
	v_mfma_f32_16x16x32_bf16 v[6:9], v[10:13], v[114:117], 0
	v_mfma_f32_16x16x32_bf16 v[122:125], v[10:13], v[98:101], 0
	v_mfma_f32_16x16x32_bf16 v[6:9], v[14:17], v[118:121], v[6:9]
	v_mfma_f32_16x16x32_bf16 v[172:175], v[14:17], v[106:109], v[122:125]
	s_setprio 0
	s_setprio 1
	v_mfma_f32_16x16x32_bf16 v[10:13], v[18:21], v[50:53], 0
	v_mfma_f32_16x16x32_bf16 v[14:17], v[22:25], v[58:61], v[10:13]
	v_mfma_f32_16x16x32_bf16 v[10:13], v[26:29], v[50:53], 0
	v_mfma_f32_16x16x32_bf16 v[176:179], v[30:33], v[58:61], v[10:13]
	v_mfma_f32_16x16x32_bf16 v[10:13], v[18:21], v[62:65], 0
	v_mfma_f32_16x16x32_bf16 v[180:183], v[22:25], v[90:93], v[10:13]
	v_mfma_f32_16x16x32_bf16 v[10:13], v[26:29], v[62:65], 0
	v_mfma_f32_16x16x32_bf16 v[184:187], v[30:33], v[90:93], v[10:13]
	v_mfma_f32_16x16x32_bf16 v[10:13], v[18:21], v[98:101], 0
	v_mfma_f32_16x16x32_bf16 v[188:191], v[22:25], v[106:109], v[10:13]
	v_mfma_f32_16x16x32_bf16 v[10:13], v[26:29], v[98:101], 0
	v_mfma_f32_16x16x32_bf16 v[192:195], v[30:33], v[106:109], v[10:13]
	v_mfma_f32_16x16x32_bf16 v[10:13], v[18:21], v[114:117], 0
	v_mfma_f32_16x16x32_bf16 v[196:199], v[22:25], v[118:121], v[10:13]
	v_mfma_f32_16x16x32_bf16 v[10:13], v[26:29], v[114:117], 0
	v_mfma_f32_16x16x32_bf16 v[200:203], v[30:33], v[118:121], v[10:13]
	s_setprio 0
	s_barrier
; template <class Epi, class Sched>
; __device__ __forceinline__ void gemm_phase(PG8_LAS unsigned char* lds, const void* wsbase, const int K, const int ldb, const Sched& S, const Epi& E) {
;     ...
;         PG8_ITER(0, PG8_FIRSTW + 2 + Epi::NVM, PG8_FIRSTW + 6 + Epi::NVM, PG8_FIRSTW + 2 + Epi::NVM, PG8_FIRSTW + 6);
;         for (int t = 2; t < nt; t += 2) PG8_ITER(t, 8 + PG8_SLK1, 8 + PG8_SLK2, 8 + PG8_SLK1, 8 + PG8_SLK2);
	s_nop 4
	ds_read_b128 v[10:13], v142
	ds_read_b128 v[22:25], v142 offset:1024
	ds_read_b128 v[30:33], v142 offset:2048
	ds_read_b128 v[204:207], v142 offset:3072
	ds_read_b128 v[208:211], v143
	ds_read_b128 v[212:215], v143 offset:1024
	ds_read_b128 v[216:219], v143 offset:2048
	ds_read_b128 v[220:223], v143 offset:3072
	s_mov_b32 m0, s40
	ds_read_b128 v[18:21], v141 offset:32768
	ds_read_b128 v[26:29], v141 offset:33792
	ds_read_b128 v[62:65], v141 offset:34816
	ds_read_b128 v[224:227], v141 offset:35840
	ds_read_b128 v[232:235], v141 offset:36864
	ds_read_b128 v[236:239], v141 offset:37888
	ds_read_b128 v[240:243], v141 offset:38912
	ds_read_b128 v[244:247], v141 offset:39936
	buffer_load_dwordx4 v136, s[12:15], s17 offen lds
	s_mov_b32 m0, s41
	s_nop 0
	buffer_load_dwordx4 v138, s[12:15], s17 offen lds
	s_waitcnt vmcnt(26)
	s_waitcnt lgkmcnt(0)
	s_barrier
	s_setprio 1
	s_waitcnt lgkmcnt(0)
	v_mfma_f32_16x16x32_bf16 v[50:53], v[10:13], v[18:21], v[66:69]
	v_mfma_f32_16x16x32_bf16 v[126:129], v[22:25], v[26:29], v[50:53]
	v_mfma_f32_16x16x32_bf16 v[50:53], v[30:33], v[18:21], v[70:73]
	v_mfma_f32_16x16x32_bf16 v[118:121], v[204:207], v[26:29], v[50:53]
	v_mfma_f32_16x16x32_bf16 v[50:53], v[10:13], v[62:65], v[74:77]
	v_mfma_f32_16x16x32_bf16 v[106:109], v[22:25], v[224:227], v[50:53]
	v_mfma_f32_16x16x32_bf16 v[50:53], v[30:33], v[62:65], v[78:81]
	v_mfma_f32_16x16x32_bf16 v[98:101], v[204:207], v[224:227], v[50:53]
	v_mfma_f32_16x16x32_bf16 v[50:53], v[10:13], v[232:235], v[82:85]
	v_mfma_f32_16x16x32_bf16 v[90:93], v[22:25], v[236:239], v[50:53]
	v_mfma_f32_16x16x32_bf16 v[50:53], v[30:33], v[232:235], v[86:89]
	v_mfma_f32_16x16x32_bf16 v[82:85], v[204:207], v[236:239], v[50:53]
	v_mfma_f32_16x16x32_bf16 v[50:53], v[10:13], v[240:243], v[94:97]
	v_mfma_f32_16x16x32_bf16 v[58:61], v[22:25], v[244:247], v[50:53]
	v_mfma_f32_16x16x32_bf16 v[50:53], v[30:33], v[240:243], v[102:105]
	v_mfma_f32_16x16x32_bf16 v[50:53], v[204:207], v[244:247], v[50:53]
	s_setprio 0
	s_setprio 1
	v_mfma_f32_16x16x32_bf16 v[66:69], v[208:211], v[18:21], v[110:113]
	v_mfma_f32_16x16x32_bf16 v[18:21], v[216:219], v[18:21], v[34:37]
	v_mfma_f32_16x16x32_bf16 v[114:117], v[220:223], v[26:29], v[18:21]
	v_mfma_f32_16x16x32_bf16 v[18:21], v[208:211], v[62:65], v[38:41]
	v_mfma_f32_16x16x32_bf16 v[110:113], v[212:215], v[224:227], v[18:21]
	v_mfma_f32_16x16x32_bf16 v[18:21], v[216:219], v[62:65], v[42:45]
	v_mfma_f32_16x16x32_bf16 v[102:105], v[220:223], v[224:227], v[18:21]
	v_mfma_f32_16x16x32_bf16 v[18:21], v[208:211], v[232:235], v[46:49]
	v_mfma_f32_16x16x32_bf16 v[94:97], v[212:215], v[236:239], v[18:21]
	v_mfma_f32_16x16x32_bf16 v[18:21], v[216:219], v[232:235], v[54:57]
	v_mfma_f32_16x16x32_bf16 v[86:89], v[220:223], v[236:239], v[18:21]
	v_mfma_f32_16x16x32_bf16 v[18:21], v[208:211], v[240:243], v[144:147]
	v_mfma_f32_16x16x32_bf16 v[62:65], v[212:215], v[244:247], v[18:21]
	v_mfma_f32_16x16x32_bf16 v[18:21], v[216:219], v[240:243], v[148:151]
	v_mfma_f32_16x16x32_bf16 v[122:125], v[212:215], v[26:29], v[66:69]
	v_mfma_f32_16x16x32_bf16 v[54:57], v[220:223], v[244:247], v[18:21]
	s_setprio 0
	s_barrier
	s_mov_b32 m0, s43
	s_add_i32 s17, s59, 0x180
	ds_read_b128 v[38:41], v141 offset:49152
	ds_read_b128 v[46:49], v141 offset:50176
	ds_read_b128 v[144:147], v141 offset:51200
	ds_read_b128 v[148:151], v141 offset:52224
	ds_read_b128 v[224:227], v141 offset:53248
	ds_read_b128 v[232:235], v141 offset:54272
	ds_read_b128 v[236:239], v141 offset:55296
	ds_read_b128 v[240:243], v141 offset:56320
	buffer_load_dwordx4 v1, s[12:15], s17 offen lds
	s_mov_b32 m0, s44
	s_nop 0
	buffer_load_dwordx4 v134, s[12:15], s17 offen lds
	s_add_i32 s17, s59, 0x10180
	s_mov_b32 m0, s47
	s_nop 0
	buffer_load_dwordx4 v1, s[12:15], s17 offen lds
	s_mov_b32 m0, s48
	s_nop 0
	buffer_load_dwordx4 v134, s[12:15], s17 offen lds
	s_mov_b32 m0, s45
	s_nop 0
	buffer_load_dwordx4 v135, s[12:15], s16 offen lds
	s_mov_b32 m0, s46
	s_nop 0
	buffer_load_dwordx4 v137, s[12:15], s16 offen lds
	s_waitcnt vmcnt(14)
	s_waitcnt lgkmcnt(0)
	s_barrier
	s_setprio 1
	s_waitcnt lgkmcnt(0)
	v_mfma_f32_16x16x32_bf16 v[18:21], v[10:13], v[38:41], v[152:155]
	v_mfma_f32_16x16x32_bf16 v[74:77], v[22:25], v[46:49], v[18:21]
	v_mfma_f32_16x16x32_bf16 v[18:21], v[30:33], v[38:41], v[156:159]
	v_mfma_f32_16x16x32_bf16 v[66:69], v[204:207], v[46:49], v[18:21]
	v_mfma_f32_16x16x32_bf16 v[18:21], v[10:13], v[144:147], v[160:163]
	v_mfma_f32_16x16x32_bf16 v[42:45], v[22:25], v[148:151], v[18:21]
	v_mfma_f32_16x16x32_bf16 v[18:21], v[30:33], v[144:147], v[164:167]
	v_mfma_f32_16x16x32_bf16 v[34:37], v[204:207], v[148:151], v[18:21]
	v_mfma_f32_16x16x32_bf16 v[18:21], v[10:13], v[224:227], v[168:171]
	v_mfma_f32_16x16x32_bf16 v[2:5], v[10:13], v[236:239], v[2:5]
	v_mfma_f32_16x16x32_bf16 v[26:29], v[22:25], v[232:235], v[18:21]
	v_mfma_f32_16x16x32_bf16 v[18:21], v[30:33], v[224:227], v[172:175]
	v_mfma_f32_16x16x32_bf16 v[10:13], v[22:25], v[240:243], v[2:5]
	v_mfma_f32_16x16x32_bf16 v[2:5], v[30:33], v[236:239], v[6:9]
	v_mfma_f32_16x16x32_bf16 v[18:21], v[204:207], v[232:235], v[18:21]
	v_mfma_f32_16x16x32_bf16 v[2:5], v[204:207], v[240:243], v[2:5]
	s_setprio 0
	s_setprio 1
	v_mfma_f32_16x16x32_bf16 v[6:9], v[208:211], v[38:41], v[14:17]
	v_mfma_f32_16x16x32_bf16 v[78:81], v[212:215], v[46:49], v[6:9]
	v_mfma_f32_16x16x32_bf16 v[6:9], v[216:219], v[38:41], v[176:179]
	v_mfma_f32_16x16x32_bf16 v[70:73], v[220:223], v[46:49], v[6:9]
	v_mfma_f32_16x16x32_bf16 v[6:9], v[208:211], v[144:147], v[180:183]
	v_mfma_f32_16x16x32_bf16 v[46:49], v[212:215], v[148:151], v[6:9]
	v_mfma_f32_16x16x32_bf16 v[6:9], v[216:219], v[144:147], v[184:187]
	v_mfma_f32_16x16x32_bf16 v[38:41], v[220:223], v[148:151], v[6:9]
	v_mfma_f32_16x16x32_bf16 v[6:9], v[208:211], v[224:227], v[188:191]
	v_mfma_f32_16x16x32_bf16 v[30:33], v[212:215], v[232:235], v[6:9]
	v_mfma_f32_16x16x32_bf16 v[6:9], v[216:219], v[224:227], v[192:195]
	v_mfma_f32_16x16x32_bf16 v[22:25], v[220:223], v[232:235], v[6:9]
	v_mfma_f32_16x16x32_bf16 v[6:9], v[208:211], v[236:239], v[196:199]
	v_mfma_f32_16x16x32_bf16 v[14:17], v[212:215], v[240:243], v[6:9]
	v_mfma_f32_16x16x32_bf16 v[6:9], v[216:219], v[236:239], v[200:203]
	v_mfma_f32_16x16x32_bf16 v[6:9], v[220:223], v[240:243], v[6:9]
	s_setprio 0
	s_barrier
	s_add_i32 s16, s59, 0x200
	s_add_i32 s17, s58, 0x200
	s_mov_b32 s58, 0
	.p2alignl 6, 3212836864

.LBB0_1633:
	ds_read_b128 v[2:5], v132
	ds_read_b128 v[6:9], v132 offset:1024
	ds_read_b128 v[10:13], v132 offset:2048
	ds_read_b128 v[14:17], v132 offset:3072
	ds_read_b128 v[18:21], v133
	ds_read_b128 v[22:25], v133 offset:1024
	ds_read_b128 v[26:29], v133 offset:2048
	ds_read_b128 v[30:33], v133 offset:3072
	s_add_i32 s15, s59, 0x100
	s_mov_b32 m0, s50
	ds_read_b128 v[34:37], v134
	ds_read_b128 v[38:41], v134 offset:1024
	ds_read_b128 v[42:45], v134 offset:2048
	ds_read_b128 v[46:49], v134 offset:3072
	ds_read_b128 v[50:53], v134 offset:4096
	ds_read_b128 v[54:57], v134 offset:5120
	ds_read_b128 v[58:61], v134 offset:6144
	ds_read_b128 v[62:65], v134 offset:7168
	buffer_load_dwordx4 v141, s[8:11], s46 offen lds
	s_mov_b32 m0, s51
	s_nop 0
	buffer_load_dwordx4 v143, s[8:11], s46 offen lds
	s_waitcnt vmcnt(18)
	s_waitcnt lgkmcnt(0)
	s_barrier
	s_setprio 1
	s_waitcnt lgkmcnt(1)
	v_mfma_f32_16x16x32_bf16 v[90:93], v[2:5], v[58:61], 0
	v_mfma_f32_16x16x32_bf16 v[66:69], v[2:5], v[34:37], 0
	v_mfma_f32_16x16x32_bf16 v[70:73], v[10:13], v[34:37], 0
	v_mfma_f32_16x16x32_bf16 v[74:77], v[2:5], v[42:45], 0
	v_mfma_f32_16x16x32_bf16 v[78:81], v[10:13], v[42:45], 0
	v_mfma_f32_16x16x32_bf16 v[82:85], v[2:5], v[50:53], 0
	v_mfma_f32_16x16x32_bf16 v[86:89], v[10:13], v[50:53], 0
	s_waitcnt lgkmcnt(0)
	v_mfma_f32_16x16x32_bf16 v[94:97], v[6:9], v[62:65], v[90:93]
	v_mfma_f32_16x16x32_bf16 v[90:93], v[10:13], v[58:61], 0
	v_mfma_f32_16x16x32_bf16 v[66:69], v[6:9], v[38:41], v[66:69]
	v_mfma_f32_16x16x32_bf16 v[70:73], v[14:17], v[38:41], v[70:73]
	v_mfma_f32_16x16x32_bf16 v[74:77], v[6:9], v[46:49], v[74:77]
	v_mfma_f32_16x16x32_bf16 v[78:81], v[14:17], v[46:49], v[78:81]
	v_mfma_f32_16x16x32_bf16 v[82:85], v[6:9], v[54:57], v[82:85]
	v_mfma_f32_16x16x32_bf16 v[86:89], v[14:17], v[54:57], v[86:89]
	v_mfma_f32_16x16x32_bf16 v[102:105], v[14:17], v[62:65], v[90:93]
	s_setprio 0
	s_setprio 1
	v_mfma_f32_16x16x32_bf16 v[90:93], v[18:21], v[34:37], 0
	v_mfma_f32_16x16x32_bf16 v[34:37], v[26:29], v[34:37], 0
	v_mfma_f32_16x16x32_bf16 v[110:113], v[22:25], v[38:41], v[90:93]
	v_mfma_f32_16x16x32_bf16 v[34:37], v[30:33], v[38:41], v[34:37]
	v_mfma_f32_16x16x32_bf16 v[38:41], v[18:21], v[42:45], 0
	v_mfma_f32_16x16x32_bf16 v[42:45], v[26:29], v[42:45], 0
	v_mfma_f32_16x16x32_bf16 v[38:41], v[22:25], v[46:49], v[38:41]
	v_mfma_f32_16x16x32_bf16 v[42:45], v[30:33], v[46:49], v[42:45]
	v_mfma_f32_16x16x32_bf16 v[46:49], v[18:21], v[50:53], 0
	v_mfma_f32_16x16x32_bf16 v[50:53], v[26:29], v[50:53], 0
	v_mfma_f32_16x16x32_bf16 v[46:49], v[22:25], v[54:57], v[46:49]
	v_mfma_f32_16x16x32_bf16 v[50:53], v[30:33], v[54:57], v[50:53]
	v_mfma_f32_16x16x32_bf16 v[54:57], v[18:21], v[58:61], 0
	v_mfma_f32_16x16x32_bf16 v[58:61], v[26:29], v[58:61], 0
	v_mfma_f32_16x16x32_bf16 v[54:57], v[22:25], v[62:65], v[54:57]
	v_mfma_f32_16x16x32_bf16 v[62:65], v[30:33], v[62:65], v[58:61]
	s_setprio 0
	s_barrier
	s_mov_b32 m0, s17
	s_nop 2
	ds_read_b128 v[58:61], v134 offset:16384
	ds_read_b128 v[90:93], v134 offset:17408
	ds_read_b128 v[98:101], v134 offset:18432
	ds_read_b128 v[106:109], v134 offset:19456
	ds_read_b128 v[114:117], v134 offset:20480
	ds_read_b128 v[118:121], v134 offset:21504
	ds_read_b128 v[122:125], v134 offset:22528
	ds_read_b128 v[126:129], v134 offset:23552
	buffer_load_dwordx4 v130, s[8:11], s15 offen lds
	s_mov_b32 m0, s18
	s_nop 0
	buffer_load_dwordx4 v131, s[8:11], s15 offen lds
	s_add_i32 s15, s59, 0x40100
	s_mov_b32 m0, s19
	s_nop 0
	buffer_load_dwordx4 v130, s[8:11], s15 offen lds
	s_mov_b32 m0, s22
	s_nop 0
	buffer_load_dwordx4 v131, s[8:11], s15 offen lds
	s_mov_b32 m0, s16
	s_nop 0
	buffer_load_dwordx4 v142, s[8:11], s52 offen lds
	s_mov_b32 m0, s23
	s_nop 0
	buffer_load_dwordx4 v144, s[8:11], s52 offen lds
	s_waitcnt vmcnt(22)
	s_waitcnt lgkmcnt(0)
	s_barrier
	s_setprio 1
	s_waitcnt lgkmcnt(7)
	v_mfma_f32_16x16x32_bf16 v[146:149], v[2:5], v[58:61], 0
	s_waitcnt lgkmcnt(5)
	v_mfma_f32_16x16x32_bf16 v[154:157], v[2:5], v[98:101], 0
	s_waitcnt lgkmcnt(3)
	v_mfma_f32_16x16x32_bf16 v[162:165], v[2:5], v[114:117], 0
	s_waitcnt lgkmcnt(1)
	v_mfma_f32_16x16x32_bf16 v[2:5], v[2:5], v[122:125], 0
	v_mfma_f32_16x16x32_bf16 v[146:149], v[6:9], v[90:93], v[146:149]
	v_mfma_f32_16x16x32_bf16 v[154:157], v[6:9], v[106:109], v[154:157]
	v_mfma_f32_16x16x32_bf16 v[162:165], v[6:9], v[118:121], v[162:165]
	s_waitcnt lgkmcnt(0)
	v_mfma_f32_16x16x32_bf16 v[2:5], v[6:9], v[126:129], v[2:5]
	v_mfma_f32_16x16x32_bf16 v[6:9], v[10:13], v[122:125], 0
	v_mfma_f32_16x16x32_bf16 v[150:153], v[10:13], v[58:61], 0
	v_mfma_f32_16x16x32_bf16 v[158:161], v[10:13], v[98:101], 0
	v_mfma_f32_16x16x32_bf16 v[166:169], v[10:13], v[114:117], 0
	v_mfma_f32_16x16x32_bf16 v[6:9], v[14:17], v[126:129], v[6:9]
	v_mfma_f32_16x16x32_bf16 v[150:153], v[14:17], v[90:93], v[150:153]
	v_mfma_f32_16x16x32_bf16 v[158:161], v[14:17], v[106:109], v[158:161]
	v_mfma_f32_16x16x32_bf16 v[166:169], v[14:17], v[118:121], v[166:169]
	s_setprio 0
	s_setprio 1
	v_mfma_f32_16x16x32_bf16 v[10:13], v[18:21], v[58:61], 0
	v_mfma_f32_16x16x32_bf16 v[14:17], v[22:25], v[90:93], v[10:13]
	v_mfma_f32_16x16x32_bf16 v[10:13], v[26:29], v[58:61], 0
	v_mfma_f32_16x16x32_bf16 v[170:173], v[30:33], v[90:93], v[10:13]
	v_mfma_f32_16x16x32_bf16 v[10:13], v[18:21], v[98:101], 0
	v_mfma_f32_16x16x32_bf16 v[174:177], v[22:25], v[106:109], v[10:13]
	v_mfma_f32_16x16x32_bf16 v[10:13], v[26:29], v[98:101], 0
	v_mfma_f32_16x16x32_bf16 v[178:181], v[30:33], v[106:109], v[10:13]
	v_mfma_f32_16x16x32_bf16 v[10:13], v[18:21], v[114:117], 0
	v_mfma_f32_16x16x32_bf16 v[182:185], v[22:25], v[118:121], v[10:13]
	v_mfma_f32_16x16x32_bf16 v[10:13], v[26:29], v[114:117], 0
	v_mfma_f32_16x16x32_bf16 v[186:189], v[30:33], v[118:121], v[10:13]
	v_mfma_f32_16x16x32_bf16 v[10:13], v[18:21], v[122:125], 0
	v_mfma_f32_16x16x32_bf16 v[190:193], v[22:25], v[126:129], v[10:13]
	v_mfma_f32_16x16x32_bf16 v[10:13], v[26:29], v[122:125], 0
	v_mfma_f32_16x16x32_bf16 v[194:197], v[30:33], v[126:129], v[10:13]
	s_setprio 0
	s_barrier
; template <class Epi, class Sched>
; __device__ __forceinline__ void gemm_phase(PG8_LAS unsigned char* lds, const void* wsbase, const int K, const int ldb, const Sched& S, const Epi& E) {
;     ...
;         PG8_ITER(0, PG8_FIRSTW + 2 + Epi::NVM, PG8_FIRSTW + 6 + Epi::NVM, PG8_FIRSTW + 2 + Epi::NVM, PG8_FIRSTW + 6);
;         for (int t = 2; t < nt; t += 2) PG8_ITER(t, 8 + PG8_SLK1, 8 + PG8_SLK2, 8 + PG8_SLK1, 8 + PG8_SLK2);
	s_nop 4
	ds_read_b128 v[10:13], v135
	ds_read_b128 v[22:25], v135 offset:1024
	ds_read_b128 v[30:33], v135 offset:2048
	ds_read_b128 v[198:201], v135 offset:3072
	ds_read_b128 v[202:205], v136
	ds_read_b128 v[206:209], v136 offset:1024
	ds_read_b128 v[210:213], v136 offset:2048
	ds_read_b128 v[214:217], v136 offset:3072
	s_mov_b32 m0, s40
	ds_read_b128 v[18:21], v134 offset:32768
	ds_read_b128 v[26:29], v134 offset:33792
	ds_read_b128 v[218:221], v134 offset:34816
	ds_read_b128 v[222:225], v134 offset:35840
	ds_read_b128 v[226:229], v134 offset:36864
	ds_read_b128 v[232:235], v134 offset:37888
	ds_read_b128 v[236:239], v134 offset:38912
	ds_read_b128 v[240:243], v134 offset:39936
	buffer_load_dwordx4 v141, s[8:11], s52 offen lds
	s_mov_b32 m0, s41
	s_nop 0
	buffer_load_dwordx4 v143, s[8:11], s52 offen lds
	s_waitcnt vmcnt(18)
	s_waitcnt lgkmcnt(0)
	s_barrier
	s_setprio 1
	s_waitcnt lgkmcnt(7)
	v_mfma_f32_16x16x32_bf16 v[58:61], v[10:13], v[18:21], v[66:69]
	s_waitcnt lgkmcnt(6)
	v_mfma_f32_16x16x32_bf16 v[122:125], v[22:25], v[26:29], v[58:61]
	v_mfma_f32_16x16x32_bf16 v[58:61], v[30:33], v[18:21], v[70:73]
	v_mfma_f32_16x16x32_bf16 v[114:117], v[198:201], v[26:29], v[58:61]
	s_waitcnt lgkmcnt(5)
	v_mfma_f32_16x16x32_bf16 v[58:61], v[10:13], v[218:221], v[74:77]
	s_waitcnt lgkmcnt(4)
	v_mfma_f32_16x16x32_bf16 v[106:109], v[22:25], v[222:225], v[58:61]
	v_mfma_f32_16x16x32_bf16 v[58:61], v[30:33], v[218:221], v[78:81]
	v_mfma_f32_16x16x32_bf16 v[98:101], v[198:201], v[222:225], v[58:61]
	s_waitcnt lgkmcnt(3)
	v_mfma_f32_16x16x32_bf16 v[58:61], v[10:13], v[226:229], v[82:85]
	s_waitcnt lgkmcnt(2)
	v_mfma_f32_16x16x32_bf16 v[90:93], v[22:25], v[232:235], v[58:61]
	v_mfma_f32_16x16x32_bf16 v[58:61], v[30:33], v[226:229], v[86:89]
	v_mfma_f32_16x16x32_bf16 v[82:85], v[198:201], v[232:235], v[58:61]
	s_waitcnt lgkmcnt(1)
	v_mfma_f32_16x16x32_bf16 v[58:61], v[10:13], v[236:239], v[94:97]
	s_waitcnt lgkmcnt(0)
	v_mfma_f32_16x16x32_bf16 v[74:77], v[22:25], v[240:243], v[58:61]
	v_mfma_f32_16x16x32_bf16 v[58:61], v[30:33], v[236:239], v[102:105]
	v_mfma_f32_16x16x32_bf16 v[58:61], v[198:201], v[240:243], v[58:61]
	s_setprio 0
	s_setprio 1
	v_mfma_f32_16x16x32_bf16 v[66:69], v[202:205], v[18:21], v[110:113]
	v_mfma_f32_16x16x32_bf16 v[18:21], v[210:213], v[18:21], v[34:37]
	v_mfma_f32_16x16x32_bf16 v[118:121], v[214:217], v[26:29], v[18:21]
	v_mfma_f32_16x16x32_bf16 v[18:21], v[202:205], v[218:221], v[38:41]
	v_mfma_f32_16x16x32_bf16 v[110:113], v[206:209], v[222:225], v[18:21]
	v_mfma_f32_16x16x32_bf16 v[18:21], v[210:213], v[218:221], v[42:45]
	v_mfma_f32_16x16x32_bf16 v[102:105], v[214:217], v[222:225], v[18:21]
	v_mfma_f32_16x16x32_bf16 v[18:21], v[202:205], v[226:229], v[46:49]
	v_mfma_f32_16x16x32_bf16 v[94:97], v[206:209], v[232:235], v[18:21]
	v_mfma_f32_16x16x32_bf16 v[18:21], v[210:213], v[226:229], v[50:53]
	v_mfma_f32_16x16x32_bf16 v[86:89], v[214:217], v[232:235], v[18:21]
	v_mfma_f32_16x16x32_bf16 v[18:21], v[202:205], v[236:239], v[54:57]
	v_mfma_f32_16x16x32_bf16 v[78:81], v[206:209], v[240:243], v[18:21]
	v_mfma_f32_16x16x32_bf16 v[18:21], v[210:213], v[236:239], v[62:65]
	v_mfma_f32_16x16x32_bf16 v[126:129], v[206:209], v[26:29], v[66:69]
	v_mfma_f32_16x16x32_bf16 v[70:73], v[214:217], v[240:243], v[18:21]
	s_setprio 0
	s_barrier
	s_mov_b32 m0, s43
	s_add_i32 s15, s59, 0x180
	ds_read_b128 v[38:41], v134 offset:49152
	ds_read_b128 v[46:49], v134 offset:50176
	ds_read_b128 v[218:221], v134 offset:51200
	ds_read_b128 v[222:225], v134 offset:52224
	ds_read_b128 v[226:229], v134 offset:53248
	ds_read_b128 v[232:235], v134 offset:54272
	ds_read_b128 v[236:239], v134 offset:55296
	ds_read_b128 v[240:243], v134 offset:56320
	buffer_load_dwordx4 v130, s[8:11], s15 offen lds
	s_mov_b32 m0, s44
	s_nop 0
	buffer_load_dwordx4 v131, s[8:11], s15 offen lds
	s_add_i32 s15, s59, 0x40180
	s_mov_b32 m0, s48
	s_nop 0
	buffer_load_dwordx4 v130, s[8:11], s15 offen lds
	s_mov_b32 m0, s49
	s_nop 0
	buffer_load_dwordx4 v131, s[8:11], s15 offen lds
	s_mov_b32 s15, 0x8800180
	s_mov_b32 m0, s45
	s_nop 0
	buffer_load_dwordx4 v142, s[8:11], s15 offen lds
	s_mov_b32 m0, s47
	s_nop 0
	buffer_load_dwordx4 v144, s[8:11], s15 offen lds
	s_waitcnt vmcnt(14)
	s_waitcnt lgkmcnt(0)
	s_barrier
	s_setprio 1
	s_waitcnt lgkmcnt(7)
	v_mfma_f32_16x16x32_bf16 v[18:21], v[10:13], v[38:41], v[146:149]
	s_waitcnt lgkmcnt(6)
	v_mfma_f32_16x16x32_bf16 v[62:65], v[22:25], v[46:49], v[18:21]
	v_mfma_f32_16x16x32_bf16 v[18:21], v[30:33], v[38:41], v[150:153]
	v_mfma_f32_16x16x32_bf16 v[50:53], v[198:201], v[46:49], v[18:21]
	s_waitcnt lgkmcnt(5)
	v_mfma_f32_16x16x32_bf16 v[18:21], v[10:13], v[218:221], v[154:157]
	s_waitcnt lgkmcnt(4)
	v_mfma_f32_16x16x32_bf16 v[42:45], v[22:25], v[222:225], v[18:21]
	v_mfma_f32_16x16x32_bf16 v[18:21], v[30:33], v[218:221], v[158:161]
	v_mfma_f32_16x16x32_bf16 v[34:37], v[198:201], v[222:225], v[18:21]
	s_waitcnt lgkmcnt(3)
	v_mfma_f32_16x16x32_bf16 v[18:21], v[10:13], v[226:229], v[162:165]
	s_waitcnt lgkmcnt(1)
	v_mfma_f32_16x16x32_bf16 v[2:5], v[10:13], v[236:239], v[2:5]
	v_mfma_f32_16x16x32_bf16 v[26:29], v[22:25], v[232:235], v[18:21]
	v_mfma_f32_16x16x32_bf16 v[18:21], v[30:33], v[226:229], v[166:169]
	s_waitcnt lgkmcnt(0)
	v_mfma_f32_16x16x32_bf16 v[10:13], v[22:25], v[240:243], v[2:5]
	v_mfma_f32_16x16x32_bf16 v[2:5], v[30:33], v[236:239], v[6:9]
	v_mfma_f32_16x16x32_bf16 v[18:21], v[198:201], v[232:235], v[18:21]
	v_mfma_f32_16x16x32_bf16 v[2:5], v[198:201], v[240:243], v[2:5]
	s_setprio 0
	s_setprio 1
	v_mfma_f32_16x16x32_bf16 v[6:9], v[202:205], v[38:41], v[14:17]
	v_mfma_f32_16x16x32_bf16 v[66:69], v[206:209], v[46:49], v[6:9]
	v_mfma_f32_16x16x32_bf16 v[6:9], v[210:213], v[38:41], v[170:173]
	v_mfma_f32_16x16x32_bf16 v[54:57], v[214:217], v[46:49], v[6:9]
	v_mfma_f32_16x16x32_bf16 v[6:9], v[202:205], v[218:221], v[174:177]
	v_mfma_f32_16x16x32_bf16 v[46:49], v[206:209], v[222:225], v[6:9]
	v_mfma_f32_16x16x32_bf16 v[6:9], v[210:213], v[218:221], v[178:181]
	v_mfma_f32_16x16x32_bf16 v[38:41], v[214:217], v[222:225], v[6:9]
	v_mfma_f32_16x16x32_bf16 v[6:9], v[202:205], v[226:229], v[182:185]
	v_mfma_f32_16x16x32_bf16 v[30:33], v[206:209], v[232:235], v[6:9]
	v_mfma_f32_16x16x32_bf16 v[6:9], v[210:213], v[226:229], v[186:189]
	v_mfma_f32_16x16x32_bf16 v[22:25], v[214:217], v[232:235], v[6:9]
	v_mfma_f32_16x16x32_bf16 v[6:9], v[202:205], v[236:239], v[190:193]
	v_mfma_f32_16x16x32_bf16 v[14:17], v[206:209], v[240:243], v[6:9]
	v_mfma_f32_16x16x32_bf16 v[6:9], v[210:213], v[236:239], v[194:197]
	v_mfma_f32_16x16x32_bf16 v[6:9], v[214:217], v[240:243], v[6:9]
	s_setprio 0
	s_barrier
	s_mov_b32 s60, 0
	.p2alignl 6, 3212836864

; #define WAIT_BAR(N) asm volatile("s_waitcnt vmcnt(" #N ") lgkmcnt(0)\n\ts_barrier":::"memory")
;   #define RESC() do{}while(0)
;   #define ROT() do{sl_prev=sl_cur;sl_cur=sl_next;sl_next=(sl_next==(NSLOT-1)*SLOTB)?0:sl_next+SLOTB;}while(0)
; template<int THRL> __device__ __forceinline__ void attn_unit(const bf16*Qu,const bf16*__restrict__ Kh,const bf16*__restrict__ Vh,bf16*Ou,const int NT,char*shm,const float kmax){
;     ...
;   int t=1;
;   for(;t+5<NT;t+=2){
;     STEP(pB0,pB1,pA0,pA1,t,true,true,true);     WAIT_BAR(3); RESC(); ROT();
;     STEP(pA0,pA1,pB0,pB1,t+1,true,true,true);   WAIT_BAR(3); RESC(); ROT();
.LBB0_1728:
	s_lshl_b32 s14, s55, 2
	s_lshl_b32 s15, s55, 17
	s_sub_i32 s14, s51, s14
	s_add_i32 s15, s15, 0xcc00000
	.p2alignl 6, 3212836864
